# speedup vs baseline: 1.0456x; 1.0456x over previous
_Z12k1_colsum_q8PKfPjPfS2_:
	s_load_dwordx8 s[4:11], s[0:1], 0x0
	v_and_b32_e32 v1, 63, v0
	v_lshrrev_b32_e32 v41, 6, v0
	s_mul_i32 s12, s2, 0xc35
	s_lshr_b32 s12, s12, 4
	v_readfirstlane_b32 s14, v41
	s_add_i32 s13, s2, 1
	s_mul_i32 s13, s13, 0xc35
	s_lshr_b32 s13, s13, 4
	s_sub_u32 s13, s13, s12
	s_sub_u32 s15, s13, 0xc0
	s_cmp_lt_u32 s14, s15
	s_cselect_b32 s29, 1, 0
	v_lshlrev_b32_e32 v34, 4, v1
	v_min_u32_e32 v35, 57, v1
	v_lshlrev_b32_e32 v35, 4, v35
	v_cmp_gt_u32_e64 s[18:19], 58, v1
	s_lshl_b32 s35, s14, 13
	s_add_u32 s36, s35, 0x1000
	v_add_u32_e32 v38, s35, v34
	v_lshrrev_b32_e32 v41, 5, v1
	v_mov_b32_e32 v42, 0xc35000
	v_mul_lo_u32 v39, v41, v42
	v_and_b32_e32 v42, 31, v1
	v_lshl_add_u32 v39, v42, 2, v39
	v_mov_b32_e32 v2, 0
	v_mov_b32_e32 v3, 0
	v_mov_b32_e32 v4, 0
	v_mov_b32_e32 v5, 0
	v_mov_b32_e32 v6, 0
	v_mov_b32_e32 v7, 0
	v_mov_b32_e32 v8, 0
	v_mov_b32_e32 v9, 0
	v_mov_b32_e32 v10, 0
	v_mov_b32_e32 v11, 0
	v_mov_b32_e32 v12, 0
	v_mov_b32_e32 v13, 0
	v_mov_b32_e32 v14, 0
	v_mov_b32_e32 v15, 0
	v_mov_b32_e32 v16, 0
	v_mov_b32_e32 v17, 0
	v_mov_b32_e32 v40, 0
	v_mov_b32_e32 v47, 0x42fe0000
	s_mov_b32 s32, 0x42fe0000
	s_mov_b32 s33, 0xc0c0400
	s_mov_b32 s34, 0x4000c0c
	s_add_u32 s15, s12, s14
	s_mul_i32 s37, s15, 0xfa0
	s_lshl_b32 s15, s15, 7
	s_waitcnt lgkmcnt(0)
	s_add_u32 s16, s4, s37
	s_addc_u32 s17, s5, 0
	s_add_u32 s40, s6, s15
	s_addc_u32 s41, s7, 0
	s_add_u32 s20, s40, 0x3c00
	s_addc_u32 s21, s41, 0
	s_add_u32 s22, s20, 0x186a000
	s_addc_u32 s23, s21, 0
	s_add_u32 s24, s22, 0x186a000
	s_addc_u32 s25, s23, 0
	s_add_u32 s26, s24, 0x186a000
	s_addc_u32 s27, s25, 0
	s_mov_b32 m0, s35
	s_nop 0
	global_load_lds_dwordx4 v34, s[16:17] nt
	global_load_lds_dwordx4 v34, s[16:17] offset:1024 nt
	global_load_lds_dwordx4 v34, s[16:17] offset:2048 nt
	global_load_lds_dwordx4 v35, s[16:17] offset:3072 nt
	s_add_u32 s16, s16, 0x7d00
	s_addc_u32 s17, s17, 0
	s_mov_b32 m0, s36
	s_nop 0
	global_load_lds_dwordx4 v34, s[16:17] nt
	global_load_lds_dwordx4 v34, s[16:17] offset:1024 nt
	global_load_lds_dwordx4 v34, s[16:17] offset:2048 nt
	global_load_lds_dwordx4 v35, s[16:17] offset:3072 nt
	s_add_u32 s16, s16, 0x7d00
	s_addc_u32 s17, s17, 0
	s_waitcnt vmcnt(4)
	ds_read_b128 v[18:21], v38 offset:0
	ds_read_b128 v[22:25], v38 offset:1024
	ds_read_b128 v[26:29], v38 offset:2048
	ds_read_b128 v[30:33], v38 offset:3072
	s_waitcnt lgkmcnt(0)
	s_mov_b32 m0, s35
	s_nop 0
	global_load_lds_dwordx4 v34, s[16:17] nt
	global_load_lds_dwordx4 v34, s[16:17] offset:1024 nt
	global_load_lds_dwordx4 v34, s[16:17] offset:2048 nt
	global_load_lds_dwordx4 v35, s[16:17] offset:3072 nt
	s_add_u32 s16, s16, 0x7d00
	s_addc_u32 s17, s17, 0
	v_cndmask_b32_e64 v30, 0, v30, s[18:19]
	v_cndmask_b32_e64 v31, 0, v31, s[18:19]
	v_cndmask_b32_e64 v32, 0, v32, s[18:19]
	v_cndmask_b32_e64 v33, 0, v33, s[18:19]
	v_max3_f32 v41, |v18|, |v19|, |v20|
	v_max3_f32 v42, |v21|, |v22|, |v23|
	v_max3_f32 v43, |v24|, |v25|, |v26|
	v_max3_f32 v44, |v27|, |v28|, |v29|
	v_max3_f32 v45, |v30|, |v31|, |v32|
	v_max3_f32 v41, v41, v42, |v33|
	v_max3_f32 v43, v43, v44, v45
	v_max_f32_e32 v41, v41, v43
	v_pk_add_f32 v[2:3], v[2:3], v[18:19]
	v_pk_add_f32 v[4:5], v[4:5], v[20:21]
	v_max_f32_dpp v41, v41, v41 quad_perm:[1,0,3,2] row_mask:0xf bank_mask:0xf
	v_pk_add_f32 v[6:7], v[6:7], v[22:23]
	v_pk_add_f32 v[8:9], v[8:9], v[24:25]
	v_max_f32_dpp v41, v41, v41 quad_perm:[2,3,0,1] row_mask:0xf bank_mask:0xf
	v_pk_add_f32 v[10:11], v[10:11], v[26:27]
	v_pk_add_f32 v[12:13], v[12:13], v[28:29]
	v_max_f32_dpp v41, v41, v41 row_half_mirror row_mask:0xf bank_mask:0xf
	v_pk_add_f32 v[14:15], v[14:15], v[30:31]
	v_pk_add_f32 v[16:17], v[16:17], v[32:33]
	v_max_f32_dpp v41, v41, v41 row_mirror row_mask:0xf bank_mask:0xf
	s_nop 1
	v_max_f32_dpp v41, v41, v41 row_bcast:15 row_mask:0xa bank_mask:0xf
	s_nop 1
	v_max_f32_dpp v41, v41, v41 row_bcast:31 row_mask:0xc bank_mask:0xf
	s_nop 1
	v_readlane_b32 s28, v41, 63
	s_nop 1
	v_div_scale_f32 v48, s[30:31], s28, s28, v47
	v_rcp_f32_e32 v49, v48
	s_nop 0
	v_fma_f32 v50, -v48, v49, 1.0
	v_fmac_f32_e32 v49, v50, v49
	v_mov_b32_e32 v50, s28
	v_div_scale_f32 v50, vcc, s32, v50, s32
	v_mul_f32_e32 v51, v50, v49
	v_fma_f32 v52, -v48, v51, v50
	v_fmac_f32_e32 v51, v52, v49
	v_fma_f32 v48, -v48, v51, v50
	v_div_fmas_f32 v48, v48, v49, v51
	v_div_fixup_f32 v48, v48, s28, v47
	v_cmp_gt_f32_e64 vcc, s28, 0
	v_writelane_b32 v40, s28, 0
	s_nop 0
	v_cndmask_b32_e32 v48, 0, v48, vcc
	v_fmaak_f32 v49, v18, v48, 0x4b400000
	v_fmaak_f32 v50, v19, v48, 0x4b400000
	v_fmaak_f32 v51, v20, v48, 0x4b400000
	v_fmaak_f32 v52, v21, v48, 0x4b400000
	v_perm_b32 v49, v50, v49, s33
	v_perm_b32 v51, v52, v51, s34
	v_or_b32_e32 v56, v49, v51
	v_fmaak_f32 v53, v22, v48, 0x4b400000
	v_fmaak_f32 v54, v23, v48, 0x4b400000
	v_fmaak_f32 v55, v24, v48, 0x4b400000
	v_fmaak_f32 v46, v25, v48, 0x4b400000
	v_perm_b32 v53, v54, v53, s33
	v_perm_b32 v55, v46, v55, s34
	v_or_b32_e32 v57, v53, v55
	v_fmaak_f32 v49, v26, v48, 0x4b400000
	v_fmaak_f32 v50, v27, v48, 0x4b400000
	v_fmaak_f32 v51, v28, v48, 0x4b400000
	v_fmaak_f32 v52, v29, v48, 0x4b400000
	v_perm_b32 v49, v50, v49, s33
	v_perm_b32 v51, v52, v51, s34
	v_or_b32_e32 v58, v49, v51
	v_fmaak_f32 v53, v30, v48, 0x4b400000
	v_fmaak_f32 v54, v31, v48, 0x4b400000
	v_fmaak_f32 v55, v32, v48, 0x4b400000
	v_fmaak_f32 v46, v33, v48, 0x4b400000
	v_perm_b32 v53, v54, v53, s33
	v_perm_b32 v55, v46, v55, s34
	v_or_b32_e32 v59, v53, v55
	s_waitcnt vmcnt(4)
	ds_read_b128 v[18:21], v38 offset:4096
	ds_read_b128 v[22:25], v38 offset:5120
	ds_read_b128 v[26:29], v38 offset:6144
	ds_read_b128 v[30:33], v38 offset:7168
	s_waitcnt lgkmcnt(0)
	s_mov_b32 m0, s36
	s_nop 0
	global_load_lds_dwordx4 v34, s[16:17] nt
	global_load_lds_dwordx4 v34, s[16:17] offset:1024 nt
	global_load_lds_dwordx4 v34, s[16:17] offset:2048 nt
	global_load_lds_dwordx4 v35, s[16:17] offset:3072 nt
	s_add_u32 s16, s16, 0x7d00
	s_addc_u32 s17, s17, 0
	v_cndmask_b32_e64 v30, 0, v30, s[18:19]
	v_cndmask_b32_e64 v31, 0, v31, s[18:19]
	v_cndmask_b32_e64 v32, 0, v32, s[18:19]
	v_cndmask_b32_e64 v33, 0, v33, s[18:19]
	v_max3_f32 v41, |v18|, |v19|, |v20|
	v_max3_f32 v42, |v21|, |v22|, |v23|
	v_max3_f32 v43, |v24|, |v25|, |v26|
	v_max3_f32 v44, |v27|, |v28|, |v29|
	v_max3_f32 v45, |v30|, |v31|, |v32|
	v_max3_f32 v41, v41, v42, |v33|
	v_max3_f32 v43, v43, v44, v45
	v_max_f32_e32 v41, v41, v43
	v_pk_add_f32 v[2:3], v[2:3], v[18:19]
	v_pk_add_f32 v[4:5], v[4:5], v[20:21]
	v_max_f32_dpp v41, v41, v41 quad_perm:[1,0,3,2] row_mask:0xf bank_mask:0xf
	v_pk_add_f32 v[6:7], v[6:7], v[22:23]
	v_pk_add_f32 v[8:9], v[8:9], v[24:25]
	v_max_f32_dpp v41, v41, v41 quad_perm:[2,3,0,1] row_mask:0xf bank_mask:0xf
	v_pk_add_f32 v[10:11], v[10:11], v[26:27]
	v_pk_add_f32 v[12:13], v[12:13], v[28:29]
	v_max_f32_dpp v41, v41, v41 row_half_mirror row_mask:0xf bank_mask:0xf
	v_pk_add_f32 v[14:15], v[14:15], v[30:31]
	v_pk_add_f32 v[16:17], v[16:17], v[32:33]
	v_max_f32_dpp v41, v41, v41 row_mirror row_mask:0xf bank_mask:0xf
	s_nop 1
	v_max_f32_dpp v41, v41, v41 row_bcast:15 row_mask:0xa bank_mask:0xf
	s_nop 1
	v_max_f32_dpp v41, v41, v41 row_bcast:31 row_mask:0xc bank_mask:0xf
	s_nop 1
	v_readlane_b32 s28, v41, 63
	s_nop 1
	v_div_scale_f32 v48, s[30:31], s28, s28, v47
	v_rcp_f32_e32 v49, v48
	s_nop 0
	v_fma_f32 v50, -v48, v49, 1.0
	v_fmac_f32_e32 v49, v50, v49
	v_mov_b32_e32 v50, s28
	v_div_scale_f32 v50, vcc, s32, v50, s32
	v_mul_f32_e32 v51, v50, v49
	v_fma_f32 v52, -v48, v51, v50
	v_fmac_f32_e32 v51, v52, v49
	v_fma_f32 v48, -v48, v51, v50
	v_div_fmas_f32 v48, v48, v49, v51
	v_div_fixup_f32 v48, v48, s28, v47
	v_cmp_gt_f32_e64 vcc, s28, 0
	v_writelane_b32 v40, s28, 1
	s_nop 0
	v_cndmask_b32_e32 v48, 0, v48, vcc
	v_fmaak_f32 v49, v18, v48, 0x4b400000
	v_fmaak_f32 v50, v19, v48, 0x4b400000
	v_fmaak_f32 v51, v20, v48, 0x4b400000
	v_fmaak_f32 v52, v21, v48, 0x4b400000
	v_perm_b32 v49, v50, v49, s33
	v_perm_b32 v51, v52, v51, s34
	v_or_b32_e32 v60, v49, v51
	v_fmaak_f32 v53, v22, v48, 0x4b400000
	v_fmaak_f32 v54, v23, v48, 0x4b400000
	v_fmaak_f32 v55, v24, v48, 0x4b400000
	v_fmaak_f32 v46, v25, v48, 0x4b400000
	v_perm_b32 v53, v54, v53, s33
	v_perm_b32 v55, v46, v55, s34
	v_or_b32_e32 v61, v53, v55
	v_fmaak_f32 v49, v26, v48, 0x4b400000
	v_fmaak_f32 v50, v27, v48, 0x4b400000
	v_fmaak_f32 v51, v28, v48, 0x4b400000
	v_fmaak_f32 v52, v29, v48, 0x4b400000
	v_perm_b32 v49, v50, v49, s33
	v_perm_b32 v51, v52, v51, s34
	v_or_b32_e32 v62, v49, v51
	v_fmaak_f32 v53, v30, v48, 0x4b400000
	v_fmaak_f32 v54, v31, v48, 0x4b400000
	v_fmaak_f32 v55, v32, v48, 0x4b400000
	v_fmaak_f32 v46, v33, v48, 0x4b400000
	v_perm_b32 v53, v54, v53, s33
	v_perm_b32 v55, v46, v55, s34
	v_or_b32_e32 v63, v53, v55
	s_waitcnt vmcnt(4)
	ds_read_b128 v[18:21], v38 offset:0
	ds_read_b128 v[22:25], v38 offset:1024
	ds_read_b128 v[26:29], v38 offset:2048
	ds_read_b128 v[30:33], v38 offset:3072
	s_waitcnt lgkmcnt(0)
	s_mov_b32 m0, s35
	s_nop 0
	global_load_lds_dwordx4 v34, s[16:17] nt
	global_load_lds_dwordx4 v34, s[16:17] offset:1024 nt
	global_load_lds_dwordx4 v34, s[16:17] offset:2048 nt
	global_load_lds_dwordx4 v35, s[16:17] offset:3072 nt
	s_add_u32 s16, s16, 0x7d00
	s_addc_u32 s17, s17, 0
	v_cndmask_b32_e64 v30, 0, v30, s[18:19]
	v_cndmask_b32_e64 v31, 0, v31, s[18:19]
	v_cndmask_b32_e64 v32, 0, v32, s[18:19]
	v_cndmask_b32_e64 v33, 0, v33, s[18:19]
	v_max3_f32 v41, |v18|, |v19|, |v20|
	v_max3_f32 v42, |v21|, |v22|, |v23|
	v_max3_f32 v43, |v24|, |v25|, |v26|
	v_max3_f32 v44, |v27|, |v28|, |v29|
	v_max3_f32 v45, |v30|, |v31|, |v32|
	v_max3_f32 v41, v41, v42, |v33|
	v_max3_f32 v43, v43, v44, v45
	v_max_f32_e32 v41, v41, v43
	v_pk_add_f32 v[2:3], v[2:3], v[18:19]
	v_pk_add_f32 v[4:5], v[4:5], v[20:21]
	v_max_f32_dpp v41, v41, v41 quad_perm:[1,0,3,2] row_mask:0xf bank_mask:0xf
	v_pk_add_f32 v[6:7], v[6:7], v[22:23]
	v_pk_add_f32 v[8:9], v[8:9], v[24:25]
	v_max_f32_dpp v41, v41, v41 quad_perm:[2,3,0,1] row_mask:0xf bank_mask:0xf
	v_pk_add_f32 v[10:11], v[10:11], v[26:27]
	v_pk_add_f32 v[12:13], v[12:13], v[28:29]
	v_max_f32_dpp v41, v41, v41 row_half_mirror row_mask:0xf bank_mask:0xf
	v_pk_add_f32 v[14:15], v[14:15], v[30:31]
	v_pk_add_f32 v[16:17], v[16:17], v[32:33]
	v_max_f32_dpp v41, v41, v41 row_mirror row_mask:0xf bank_mask:0xf
	s_nop 1
	v_max_f32_dpp v41, v41, v41 row_bcast:15 row_mask:0xa bank_mask:0xf
	s_nop 1
	v_max_f32_dpp v41, v41, v41 row_bcast:31 row_mask:0xc bank_mask:0xf
	s_nop 1
	v_readlane_b32 s28, v41, 63
	s_nop 1
	v_div_scale_f32 v48, s[30:31], s28, s28, v47
	v_rcp_f32_e32 v49, v48
	s_nop 0
	v_fma_f32 v50, -v48, v49, 1.0
	v_fmac_f32_e32 v49, v50, v49
	v_mov_b32_e32 v50, s28
	v_div_scale_f32 v50, vcc, s32, v50, s32
	v_mul_f32_e32 v51, v50, v49
	v_fma_f32 v52, -v48, v51, v50
	v_fmac_f32_e32 v51, v52, v49
	v_fma_f32 v48, -v48, v51, v50
	v_div_fmas_f32 v48, v48, v49, v51
	v_div_fixup_f32 v48, v48, s28, v47
	v_cmp_gt_f32_e64 vcc, s28, 0
	v_writelane_b32 v40, s28, 2
	s_nop 0
	v_cndmask_b32_e32 v48, 0, v48, vcc
	v_fmaak_f32 v49, v18, v48, 0x4b400000
	v_fmaak_f32 v50, v19, v48, 0x4b400000
	v_fmaak_f32 v51, v20, v48, 0x4b400000
	v_fmaak_f32 v52, v21, v48, 0x4b400000
	v_perm_b32 v49, v50, v49, s33
	v_perm_b32 v51, v52, v51, s34
	v_or_b32_e32 v64, v49, v51
	v_fmaak_f32 v53, v22, v48, 0x4b400000
	v_fmaak_f32 v54, v23, v48, 0x4b400000
	v_fmaak_f32 v55, v24, v48, 0x4b400000
	v_fmaak_f32 v46, v25, v48, 0x4b400000
	v_perm_b32 v53, v54, v53, s33
	v_perm_b32 v55, v46, v55, s34
	v_or_b32_e32 v65, v53, v55
	v_fmaak_f32 v49, v26, v48, 0x4b400000
	v_fmaak_f32 v50, v27, v48, 0x4b400000
	v_fmaak_f32 v51, v28, v48, 0x4b400000
	v_fmaak_f32 v52, v29, v48, 0x4b400000
	v_perm_b32 v49, v50, v49, s33
	v_perm_b32 v51, v52, v51, s34
	v_or_b32_e32 v66, v49, v51
	v_fmaak_f32 v53, v30, v48, 0x4b400000
	v_fmaak_f32 v54, v31, v48, 0x4b400000
	v_fmaak_f32 v55, v32, v48, 0x4b400000
	v_fmaak_f32 v46, v33, v48, 0x4b400000
	v_perm_b32 v53, v54, v53, s33
	v_perm_b32 v55, v46, v55, s34
	v_or_b32_e32 v67, v53, v55
	s_waitcnt vmcnt(4)
	ds_read_b128 v[18:21], v38 offset:4096
	ds_read_b128 v[22:25], v38 offset:5120
	ds_read_b128 v[26:29], v38 offset:6144
	ds_read_b128 v[30:33], v38 offset:7168
	s_waitcnt lgkmcnt(0)
	s_mov_b32 m0, s36
	s_nop 0
	global_load_lds_dwordx4 v34, s[16:17] nt
	global_load_lds_dwordx4 v34, s[16:17] offset:1024 nt
	global_load_lds_dwordx4 v34, s[16:17] offset:2048 nt
	global_load_lds_dwordx4 v35, s[16:17] offset:3072 nt
	s_add_u32 s16, s16, 0x7d00
	s_addc_u32 s17, s17, 0
	v_cndmask_b32_e64 v30, 0, v30, s[18:19]
	v_cndmask_b32_e64 v31, 0, v31, s[18:19]
	v_cndmask_b32_e64 v32, 0, v32, s[18:19]
	v_cndmask_b32_e64 v33, 0, v33, s[18:19]
	v_max3_f32 v41, |v18|, |v19|, |v20|
	v_max3_f32 v42, |v21|, |v22|, |v23|
	v_max3_f32 v43, |v24|, |v25|, |v26|
	v_max3_f32 v44, |v27|, |v28|, |v29|
	v_max3_f32 v45, |v30|, |v31|, |v32|
	v_max3_f32 v41, v41, v42, |v33|
	v_max3_f32 v43, v43, v44, v45
	v_max_f32_e32 v41, v41, v43
	v_pk_add_f32 v[2:3], v[2:3], v[18:19]
	v_pk_add_f32 v[4:5], v[4:5], v[20:21]
	v_max_f32_dpp v41, v41, v41 quad_perm:[1,0,3,2] row_mask:0xf bank_mask:0xf
	v_pk_add_f32 v[6:7], v[6:7], v[22:23]
	v_pk_add_f32 v[8:9], v[8:9], v[24:25]
	v_max_f32_dpp v41, v41, v41 quad_perm:[2,3,0,1] row_mask:0xf bank_mask:0xf
	v_pk_add_f32 v[10:11], v[10:11], v[26:27]
	v_pk_add_f32 v[12:13], v[12:13], v[28:29]
	v_max_f32_dpp v41, v41, v41 row_half_mirror row_mask:0xf bank_mask:0xf
	v_pk_add_f32 v[14:15], v[14:15], v[30:31]
	v_pk_add_f32 v[16:17], v[16:17], v[32:33]
	v_max_f32_dpp v41, v41, v41 row_mirror row_mask:0xf bank_mask:0xf
	s_nop 1
	v_max_f32_dpp v41, v41, v41 row_bcast:15 row_mask:0xa bank_mask:0xf
	s_nop 1
	v_max_f32_dpp v41, v41, v41 row_bcast:31 row_mask:0xc bank_mask:0xf
	s_nop 1
	v_readlane_b32 s28, v41, 63
	s_nop 1
	v_div_scale_f32 v48, s[30:31], s28, s28, v47
	v_rcp_f32_e32 v49, v48
	s_nop 0
	v_fma_f32 v50, -v48, v49, 1.0
	v_fmac_f32_e32 v49, v50, v49
	v_mov_b32_e32 v50, s28
	v_div_scale_f32 v50, vcc, s32, v50, s32
	v_mul_f32_e32 v51, v50, v49
	v_fma_f32 v52, -v48, v51, v50
	v_fmac_f32_e32 v51, v52, v49
	v_fma_f32 v48, -v48, v51, v50
	v_div_fmas_f32 v48, v48, v49, v51
	v_div_fixup_f32 v48, v48, s28, v47
	v_cmp_gt_f32_e64 vcc, s28, 0
	v_writelane_b32 v40, s28, 3
	s_nop 0
	v_cndmask_b32_e32 v48, 0, v48, vcc
	v_fmaak_f32 v49, v18, v48, 0x4b400000
	v_fmaak_f32 v50, v19, v48, 0x4b400000
	v_fmaak_f32 v51, v20, v48, 0x4b400000
	v_fmaak_f32 v52, v21, v48, 0x4b400000
	v_perm_b32 v49, v50, v49, s33
	v_perm_b32 v51, v52, v51, s34
	v_or_b32_e32 v68, v49, v51
	v_fmaak_f32 v53, v22, v48, 0x4b400000
	v_fmaak_f32 v54, v23, v48, 0x4b400000
	v_fmaak_f32 v55, v24, v48, 0x4b400000
	v_fmaak_f32 v46, v25, v48, 0x4b400000
	v_perm_b32 v53, v54, v53, s33
	v_perm_b32 v55, v46, v55, s34
	v_or_b32_e32 v69, v53, v55
	v_fmaak_f32 v49, v26, v48, 0x4b400000
	v_fmaak_f32 v50, v27, v48, 0x4b400000
	v_fmaak_f32 v51, v28, v48, 0x4b400000
	v_fmaak_f32 v52, v29, v48, 0x4b400000
	v_perm_b32 v49, v50, v49, s33
	v_perm_b32 v51, v52, v51, s34
	v_or_b32_e32 v70, v49, v51
	v_fmaak_f32 v53, v30, v48, 0x4b400000
	v_fmaak_f32 v54, v31, v48, 0x4b400000
	v_fmaak_f32 v55, v32, v48, 0x4b400000
	v_fmaak_f32 v46, v33, v48, 0x4b400000
	v_perm_b32 v53, v54, v53, s33
	v_perm_b32 v55, v46, v55, s34
	v_or_b32_e32 v71, v53, v55
	s_waitcnt vmcnt(4)
	ds_read_b128 v[18:21], v38 offset:0
	ds_read_b128 v[22:25], v38 offset:1024
	ds_read_b128 v[26:29], v38 offset:2048
	ds_read_b128 v[30:33], v38 offset:3072
	s_waitcnt lgkmcnt(0)
	s_mov_b32 m0, s35
	s_nop 0
	global_load_lds_dwordx4 v34, s[16:17] nt
	global_load_lds_dwordx4 v34, s[16:17] offset:1024 nt
	global_load_lds_dwordx4 v34, s[16:17] offset:2048 nt
	global_load_lds_dwordx4 v35, s[16:17] offset:3072 nt
	s_add_u32 s16, s16, 0x7d00
	s_addc_u32 s17, s17, 0
	v_cndmask_b32_e64 v30, 0, v30, s[18:19]
	v_cndmask_b32_e64 v31, 0, v31, s[18:19]
	v_cndmask_b32_e64 v32, 0, v32, s[18:19]
	v_cndmask_b32_e64 v33, 0, v33, s[18:19]
	v_max3_f32 v41, |v18|, |v19|, |v20|
	v_max3_f32 v42, |v21|, |v22|, |v23|
	v_max3_f32 v43, |v24|, |v25|, |v26|
	v_max3_f32 v44, |v27|, |v28|, |v29|
	v_max3_f32 v45, |v30|, |v31|, |v32|
	v_max3_f32 v41, v41, v42, |v33|
	v_max3_f32 v43, v43, v44, v45
	v_max_f32_e32 v41, v41, v43
	v_pk_add_f32 v[2:3], v[2:3], v[18:19]
	v_pk_add_f32 v[4:5], v[4:5], v[20:21]
	v_max_f32_dpp v41, v41, v41 quad_perm:[1,0,3,2] row_mask:0xf bank_mask:0xf
	v_pk_add_f32 v[6:7], v[6:7], v[22:23]
	v_pk_add_f32 v[8:9], v[8:9], v[24:25]
	v_max_f32_dpp v41, v41, v41 quad_perm:[2,3,0,1] row_mask:0xf bank_mask:0xf
	v_pk_add_f32 v[10:11], v[10:11], v[26:27]
	v_pk_add_f32 v[12:13], v[12:13], v[28:29]
	v_max_f32_dpp v41, v41, v41 row_half_mirror row_mask:0xf bank_mask:0xf
	v_pk_add_f32 v[14:15], v[14:15], v[30:31]
	v_pk_add_f32 v[16:17], v[16:17], v[32:33]
	v_max_f32_dpp v41, v41, v41 row_mirror row_mask:0xf bank_mask:0xf
	s_nop 1
	v_max_f32_dpp v41, v41, v41 row_bcast:15 row_mask:0xa bank_mask:0xf
	s_nop 1
	v_max_f32_dpp v41, v41, v41 row_bcast:31 row_mask:0xc bank_mask:0xf
	s_nop 1
	v_readlane_b32 s28, v41, 63
	s_nop 1
	v_div_scale_f32 v48, s[30:31], s28, s28, v47
	v_rcp_f32_e32 v49, v48
	s_nop 0
	v_fma_f32 v50, -v48, v49, 1.0
	v_fmac_f32_e32 v49, v50, v49
	v_mov_b32_e32 v50, s28
	v_div_scale_f32 v50, vcc, s32, v50, s32
	v_mul_f32_e32 v51, v50, v49
	v_fma_f32 v52, -v48, v51, v50
	v_fmac_f32_e32 v51, v52, v49
	v_fma_f32 v48, -v48, v51, v50
	v_div_fmas_f32 v48, v48, v49, v51
	v_div_fixup_f32 v48, v48, s28, v47
	v_cmp_gt_f32_e64 vcc, s28, 0
	v_writelane_b32 v40, s28, 4
	s_nop 0
	v_cndmask_b32_e32 v48, 0, v48, vcc
	v_fmaak_f32 v49, v18, v48, 0x4b400000
	v_fmaak_f32 v50, v19, v48, 0x4b400000
	v_fmaak_f32 v51, v20, v48, 0x4b400000
	v_fmaak_f32 v52, v21, v48, 0x4b400000
	v_perm_b32 v49, v50, v49, s33
	v_perm_b32 v51, v52, v51, s34
	v_or_b32_e32 v72, v49, v51
	v_fmaak_f32 v53, v22, v48, 0x4b400000
	v_fmaak_f32 v54, v23, v48, 0x4b400000
	v_fmaak_f32 v55, v24, v48, 0x4b400000
	v_fmaak_f32 v46, v25, v48, 0x4b400000
	v_perm_b32 v53, v54, v53, s33
	v_perm_b32 v55, v46, v55, s34
	v_or_b32_e32 v73, v53, v55
	v_fmaak_f32 v49, v26, v48, 0x4b400000
	v_fmaak_f32 v50, v27, v48, 0x4b400000
	v_fmaak_f32 v51, v28, v48, 0x4b400000
	v_fmaak_f32 v52, v29, v48, 0x4b400000
	v_perm_b32 v49, v50, v49, s33
	v_perm_b32 v51, v52, v51, s34
	v_or_b32_e32 v74, v49, v51
	v_fmaak_f32 v53, v30, v48, 0x4b400000
	v_fmaak_f32 v54, v31, v48, 0x4b400000
	v_fmaak_f32 v55, v32, v48, 0x4b400000
	v_fmaak_f32 v46, v33, v48, 0x4b400000
	v_perm_b32 v53, v54, v53, s33
	v_perm_b32 v55, v46, v55, s34
	v_or_b32_e32 v75, v53, v55
	s_waitcnt vmcnt(4)
	ds_read_b128 v[18:21], v38 offset:4096
	ds_read_b128 v[22:25], v38 offset:5120
	ds_read_b128 v[26:29], v38 offset:6144
	ds_read_b128 v[30:33], v38 offset:7168
	s_waitcnt lgkmcnt(0)
	s_mov_b32 m0, s36
	s_nop 0
	global_load_lds_dwordx4 v34, s[16:17] nt
	global_load_lds_dwordx4 v34, s[16:17] offset:1024 nt
	global_load_lds_dwordx4 v34, s[16:17] offset:2048 nt
	global_load_lds_dwordx4 v35, s[16:17] offset:3072 nt
	s_add_u32 s16, s16, 0x7d00
	s_addc_u32 s17, s17, 0
	v_cndmask_b32_e64 v30, 0, v30, s[18:19]
	v_cndmask_b32_e64 v31, 0, v31, s[18:19]
	v_cndmask_b32_e64 v32, 0, v32, s[18:19]
	v_cndmask_b32_e64 v33, 0, v33, s[18:19]
	v_max3_f32 v41, |v18|, |v19|, |v20|
	v_max3_f32 v42, |v21|, |v22|, |v23|
	v_max3_f32 v43, |v24|, |v25|, |v26|
	v_max3_f32 v44, |v27|, |v28|, |v29|
	v_max3_f32 v45, |v30|, |v31|, |v32|
	v_max3_f32 v41, v41, v42, |v33|
	v_max3_f32 v43, v43, v44, v45
	v_max_f32_e32 v41, v41, v43
	v_pk_add_f32 v[2:3], v[2:3], v[18:19]
	v_pk_add_f32 v[4:5], v[4:5], v[20:21]
	v_max_f32_dpp v41, v41, v41 quad_perm:[1,0,3,2] row_mask:0xf bank_mask:0xf
	v_pk_add_f32 v[6:7], v[6:7], v[22:23]
	v_pk_add_f32 v[8:9], v[8:9], v[24:25]
	v_max_f32_dpp v41, v41, v41 quad_perm:[2,3,0,1] row_mask:0xf bank_mask:0xf
	v_pk_add_f32 v[10:11], v[10:11], v[26:27]
	v_pk_add_f32 v[12:13], v[12:13], v[28:29]
	v_max_f32_dpp v41, v41, v41 row_half_mirror row_mask:0xf bank_mask:0xf
	v_pk_add_f32 v[14:15], v[14:15], v[30:31]
	v_pk_add_f32 v[16:17], v[16:17], v[32:33]
	v_max_f32_dpp v41, v41, v41 row_mirror row_mask:0xf bank_mask:0xf
	s_nop 1
	v_max_f32_dpp v41, v41, v41 row_bcast:15 row_mask:0xa bank_mask:0xf
	s_nop 1
	v_max_f32_dpp v41, v41, v41 row_bcast:31 row_mask:0xc bank_mask:0xf
	s_nop 1
	v_readlane_b32 s28, v41, 63
	s_nop 1
	v_div_scale_f32 v48, s[30:31], s28, s28, v47
	v_rcp_f32_e32 v49, v48
	s_nop 0
	v_fma_f32 v50, -v48, v49, 1.0
	v_fmac_f32_e32 v49, v50, v49
	v_mov_b32_e32 v50, s28
	v_div_scale_f32 v50, vcc, s32, v50, s32
	v_mul_f32_e32 v51, v50, v49
	v_fma_f32 v52, -v48, v51, v50
	v_fmac_f32_e32 v51, v52, v49
	v_fma_f32 v48, -v48, v51, v50
	v_div_fmas_f32 v48, v48, v49, v51
	v_div_fixup_f32 v48, v48, s28, v47
	v_cmp_gt_f32_e64 vcc, s28, 0
	v_writelane_b32 v40, s28, 5
	s_nop 0
	v_cndmask_b32_e32 v48, 0, v48, vcc
	v_fmaak_f32 v49, v18, v48, 0x4b400000
	v_fmaak_f32 v50, v19, v48, 0x4b400000
	v_fmaak_f32 v51, v20, v48, 0x4b400000
	v_fmaak_f32 v52, v21, v48, 0x4b400000
	v_perm_b32 v49, v50, v49, s33
	v_perm_b32 v51, v52, v51, s34
	v_or_b32_e32 v76, v49, v51
	v_fmaak_f32 v53, v22, v48, 0x4b400000
	v_fmaak_f32 v54, v23, v48, 0x4b400000
	v_fmaak_f32 v55, v24, v48, 0x4b400000
	v_fmaak_f32 v46, v25, v48, 0x4b400000
	v_perm_b32 v53, v54, v53, s33
	v_perm_b32 v55, v46, v55, s34
	v_or_b32_e32 v77, v53, v55
	v_fmaak_f32 v49, v26, v48, 0x4b400000
	v_fmaak_f32 v50, v27, v48, 0x4b400000
	v_fmaak_f32 v51, v28, v48, 0x4b400000
	v_fmaak_f32 v52, v29, v48, 0x4b400000
	v_perm_b32 v49, v50, v49, s33
	v_perm_b32 v51, v52, v51, s34
	v_or_b32_e32 v78, v49, v51
	v_fmaak_f32 v53, v30, v48, 0x4b400000
	v_fmaak_f32 v54, v31, v48, 0x4b400000
	v_fmaak_f32 v55, v32, v48, 0x4b400000
	v_fmaak_f32 v46, v33, v48, 0x4b400000
	v_perm_b32 v53, v54, v53, s33
	v_perm_b32 v55, v46, v55, s34
	v_or_b32_e32 v79, v53, v55
	s_waitcnt vmcnt(4)
	ds_read_b128 v[18:21], v38 offset:0
	ds_read_b128 v[22:25], v38 offset:1024
	ds_read_b128 v[26:29], v38 offset:2048
	ds_read_b128 v[30:33], v38 offset:3072
	s_waitcnt lgkmcnt(0)
	s_mov_b32 m0, s35
	s_nop 0
	global_load_lds_dwordx4 v34, s[16:17] nt
	global_load_lds_dwordx4 v34, s[16:17] offset:1024 nt
	global_load_lds_dwordx4 v34, s[16:17] offset:2048 nt
	global_load_lds_dwordx4 v35, s[16:17] offset:3072 nt
	s_add_u32 s16, s16, 0x7d00
	s_addc_u32 s17, s17, 0
	v_cndmask_b32_e64 v30, 0, v30, s[18:19]
	v_cndmask_b32_e64 v31, 0, v31, s[18:19]
	v_cndmask_b32_e64 v32, 0, v32, s[18:19]
	v_cndmask_b32_e64 v33, 0, v33, s[18:19]
	v_max3_f32 v41, |v18|, |v19|, |v20|
	v_max3_f32 v42, |v21|, |v22|, |v23|
	v_max3_f32 v43, |v24|, |v25|, |v26|
	v_max3_f32 v44, |v27|, |v28|, |v29|
	v_max3_f32 v45, |v30|, |v31|, |v32|
	v_max3_f32 v41, v41, v42, |v33|
	v_max3_f32 v43, v43, v44, v45
	v_max_f32_e32 v41, v41, v43
	v_pk_add_f32 v[2:3], v[2:3], v[18:19]
	v_pk_add_f32 v[4:5], v[4:5], v[20:21]
	v_max_f32_dpp v41, v41, v41 quad_perm:[1,0,3,2] row_mask:0xf bank_mask:0xf
	v_pk_add_f32 v[6:7], v[6:7], v[22:23]
	v_pk_add_f32 v[8:9], v[8:9], v[24:25]
	v_max_f32_dpp v41, v41, v41 quad_perm:[2,3,0,1] row_mask:0xf bank_mask:0xf
	v_pk_add_f32 v[10:11], v[10:11], v[26:27]
	v_pk_add_f32 v[12:13], v[12:13], v[28:29]
	v_max_f32_dpp v41, v41, v41 row_half_mirror row_mask:0xf bank_mask:0xf
	v_pk_add_f32 v[14:15], v[14:15], v[30:31]
	v_pk_add_f32 v[16:17], v[16:17], v[32:33]
	v_max_f32_dpp v41, v41, v41 row_mirror row_mask:0xf bank_mask:0xf
	s_nop 1
	v_max_f32_dpp v41, v41, v41 row_bcast:15 row_mask:0xa bank_mask:0xf
	s_nop 1
	v_max_f32_dpp v41, v41, v41 row_bcast:31 row_mask:0xc bank_mask:0xf
	s_nop 1
	v_readlane_b32 s28, v41, 63
	s_nop 1
	v_div_scale_f32 v48, s[30:31], s28, s28, v47
	v_rcp_f32_e32 v49, v48
	s_nop 0
	v_fma_f32 v50, -v48, v49, 1.0
	v_fmac_f32_e32 v49, v50, v49
	v_mov_b32_e32 v50, s28
	v_div_scale_f32 v50, vcc, s32, v50, s32
	v_mul_f32_e32 v51, v50, v49
	v_fma_f32 v52, -v48, v51, v50
	v_fmac_f32_e32 v51, v52, v49
	v_fma_f32 v48, -v48, v51, v50
	v_div_fmas_f32 v48, v48, v49, v51
	v_div_fixup_f32 v48, v48, s28, v47
	v_cmp_gt_f32_e64 vcc, s28, 0
	v_writelane_b32 v40, s28, 6
	s_nop 0
	v_cndmask_b32_e32 v48, 0, v48, vcc
	v_fmaak_f32 v49, v18, v48, 0x4b400000
	v_fmaak_f32 v50, v19, v48, 0x4b400000
	v_fmaak_f32 v51, v20, v48, 0x4b400000
	v_fmaak_f32 v52, v21, v48, 0x4b400000
	v_perm_b32 v49, v50, v49, s33
	v_perm_b32 v51, v52, v51, s34
	v_or_b32_e32 v80, v49, v51
	v_fmaak_f32 v53, v22, v48, 0x4b400000
	v_fmaak_f32 v54, v23, v48, 0x4b400000
	v_fmaak_f32 v55, v24, v48, 0x4b400000
	v_fmaak_f32 v46, v25, v48, 0x4b400000
	v_perm_b32 v53, v54, v53, s33
	v_perm_b32 v55, v46, v55, s34
	v_or_b32_e32 v81, v53, v55
	v_fmaak_f32 v49, v26, v48, 0x4b400000
	v_fmaak_f32 v50, v27, v48, 0x4b400000
	v_fmaak_f32 v51, v28, v48, 0x4b400000
	v_fmaak_f32 v52, v29, v48, 0x4b400000
	v_perm_b32 v49, v50, v49, s33
	v_perm_b32 v51, v52, v51, s34
	v_or_b32_e32 v82, v49, v51
	v_fmaak_f32 v53, v30, v48, 0x4b400000
	v_fmaak_f32 v54, v31, v48, 0x4b400000
	v_fmaak_f32 v55, v32, v48, 0x4b400000
	v_fmaak_f32 v46, v33, v48, 0x4b400000
	v_perm_b32 v53, v54, v53, s33
	v_perm_b32 v55, v46, v55, s34
	v_or_b32_e32 v83, v53, v55
	s_waitcnt vmcnt(4)
	ds_read_b128 v[18:21], v38 offset:4096
	ds_read_b128 v[22:25], v38 offset:5120
	ds_read_b128 v[26:29], v38 offset:6144
	ds_read_b128 v[30:33], v38 offset:7168
	s_waitcnt lgkmcnt(0)
	s_mov_b32 m0, s36
	s_nop 0
	global_load_lds_dwordx4 v34, s[16:17] nt
	global_load_lds_dwordx4 v34, s[16:17] offset:1024 nt
	global_load_lds_dwordx4 v34, s[16:17] offset:2048 nt
	global_load_lds_dwordx4 v35, s[16:17] offset:3072 nt
	s_add_u32 s16, s16, 0x7d00
	s_addc_u32 s17, s17, 0
	v_cndmask_b32_e64 v30, 0, v30, s[18:19]
	v_cndmask_b32_e64 v31, 0, v31, s[18:19]
	v_cndmask_b32_e64 v32, 0, v32, s[18:19]
	v_cndmask_b32_e64 v33, 0, v33, s[18:19]
	v_max3_f32 v41, |v18|, |v19|, |v20|
	v_max3_f32 v42, |v21|, |v22|, |v23|
	v_max3_f32 v43, |v24|, |v25|, |v26|
	v_max3_f32 v44, |v27|, |v28|, |v29|
	v_max3_f32 v45, |v30|, |v31|, |v32|
	v_max3_f32 v41, v41, v42, |v33|
	v_max3_f32 v43, v43, v44, v45
	v_max_f32_e32 v41, v41, v43
	v_pk_add_f32 v[2:3], v[2:3], v[18:19]
	v_pk_add_f32 v[4:5], v[4:5], v[20:21]
	v_max_f32_dpp v41, v41, v41 quad_perm:[1,0,3,2] row_mask:0xf bank_mask:0xf
	v_pk_add_f32 v[6:7], v[6:7], v[22:23]
	v_pk_add_f32 v[8:9], v[8:9], v[24:25]
	v_max_f32_dpp v41, v41, v41 quad_perm:[2,3,0,1] row_mask:0xf bank_mask:0xf
	v_pk_add_f32 v[10:11], v[10:11], v[26:27]
	v_pk_add_f32 v[12:13], v[12:13], v[28:29]
	v_max_f32_dpp v41, v41, v41 row_half_mirror row_mask:0xf bank_mask:0xf
	v_pk_add_f32 v[14:15], v[14:15], v[30:31]
	v_pk_add_f32 v[16:17], v[16:17], v[32:33]
	v_max_f32_dpp v41, v41, v41 row_mirror row_mask:0xf bank_mask:0xf
	s_nop 1
	v_max_f32_dpp v41, v41, v41 row_bcast:15 row_mask:0xa bank_mask:0xf
	s_nop 1
	v_max_f32_dpp v41, v41, v41 row_bcast:31 row_mask:0xc bank_mask:0xf
	s_nop 1
	v_readlane_b32 s28, v41, 63
	s_nop 1
	v_div_scale_f32 v48, s[30:31], s28, s28, v47
	v_rcp_f32_e32 v49, v48
	s_nop 0
	v_fma_f32 v50, -v48, v49, 1.0
	v_fmac_f32_e32 v49, v50, v49
	v_mov_b32_e32 v50, s28
	v_div_scale_f32 v50, vcc, s32, v50, s32
	v_mul_f32_e32 v51, v50, v49
	v_fma_f32 v52, -v48, v51, v50
	v_fmac_f32_e32 v51, v52, v49
	v_fma_f32 v48, -v48, v51, v50
	v_div_fmas_f32 v48, v48, v49, v51
	v_div_fixup_f32 v48, v48, s28, v47
	v_cmp_gt_f32_e64 vcc, s28, 0
	v_writelane_b32 v40, s28, 7
	s_nop 0
	v_cndmask_b32_e32 v48, 0, v48, vcc
	v_fmaak_f32 v49, v18, v48, 0x4b400000
	v_fmaak_f32 v50, v19, v48, 0x4b400000
	v_fmaak_f32 v51, v20, v48, 0x4b400000
	v_fmaak_f32 v52, v21, v48, 0x4b400000
	v_perm_b32 v49, v50, v49, s33
	v_perm_b32 v51, v52, v51, s34
	v_or_b32_e32 v84, v49, v51
	v_fmaak_f32 v53, v22, v48, 0x4b400000
	v_fmaak_f32 v54, v23, v48, 0x4b400000
	v_fmaak_f32 v55, v24, v48, 0x4b400000
	v_fmaak_f32 v46, v25, v48, 0x4b400000
	v_perm_b32 v53, v54, v53, s33
	v_perm_b32 v55, v46, v55, s34
	v_or_b32_e32 v85, v53, v55
	v_fmaak_f32 v49, v26, v48, 0x4b400000
	v_fmaak_f32 v50, v27, v48, 0x4b400000
	v_fmaak_f32 v51, v28, v48, 0x4b400000
	v_fmaak_f32 v52, v29, v48, 0x4b400000
	v_perm_b32 v49, v50, v49, s33
	v_perm_b32 v51, v52, v51, s34
	v_or_b32_e32 v86, v49, v51
	v_fmaak_f32 v53, v30, v48, 0x4b400000
	v_fmaak_f32 v54, v31, v48, 0x4b400000
	v_fmaak_f32 v55, v32, v48, 0x4b400000
	v_fmaak_f32 v46, v33, v48, 0x4b400000
	v_perm_b32 v53, v54, v53, s33
	v_perm_b32 v55, v46, v55, s34
	v_or_b32_e32 v87, v53, v55
	s_waitcnt vmcnt(4)
	ds_read_b128 v[18:21], v38 offset:0
	ds_read_b128 v[22:25], v38 offset:1024
	ds_read_b128 v[26:29], v38 offset:2048
	ds_read_b128 v[30:33], v38 offset:3072
	s_waitcnt lgkmcnt(0)
	s_mov_b32 m0, s35
	s_nop 0
	global_load_lds_dwordx4 v34, s[16:17] nt
	global_load_lds_dwordx4 v34, s[16:17] offset:1024 nt
	global_load_lds_dwordx4 v34, s[16:17] offset:2048 nt
	global_load_lds_dwordx4 v35, s[16:17] offset:3072 nt
	s_add_u32 s16, s16, 0x7d00
	s_addc_u32 s17, s17, 0
	v_cndmask_b32_e64 v30, 0, v30, s[18:19]
	v_cndmask_b32_e64 v31, 0, v31, s[18:19]
	v_cndmask_b32_e64 v32, 0, v32, s[18:19]
	v_cndmask_b32_e64 v33, 0, v33, s[18:19]
	v_max3_f32 v41, |v18|, |v19|, |v20|
	v_max3_f32 v42, |v21|, |v22|, |v23|
	v_max3_f32 v43, |v24|, |v25|, |v26|
	v_max3_f32 v44, |v27|, |v28|, |v29|
	v_max3_f32 v45, |v30|, |v31|, |v32|
	v_max3_f32 v41, v41, v42, |v33|
	v_max3_f32 v43, v43, v44, v45
	v_max_f32_e32 v41, v41, v43
	v_pk_add_f32 v[2:3], v[2:3], v[18:19]
	v_pk_add_f32 v[4:5], v[4:5], v[20:21]
	v_max_f32_dpp v41, v41, v41 quad_perm:[1,0,3,2] row_mask:0xf bank_mask:0xf
	v_pk_add_f32 v[6:7], v[6:7], v[22:23]
	v_pk_add_f32 v[8:9], v[8:9], v[24:25]
	v_max_f32_dpp v41, v41, v41 quad_perm:[2,3,0,1] row_mask:0xf bank_mask:0xf
	v_pk_add_f32 v[10:11], v[10:11], v[26:27]
	v_pk_add_f32 v[12:13], v[12:13], v[28:29]
	v_max_f32_dpp v41, v41, v41 row_half_mirror row_mask:0xf bank_mask:0xf
	v_pk_add_f32 v[14:15], v[14:15], v[30:31]
	v_pk_add_f32 v[16:17], v[16:17], v[32:33]
	v_max_f32_dpp v41, v41, v41 row_mirror row_mask:0xf bank_mask:0xf
	s_nop 1
	v_max_f32_dpp v41, v41, v41 row_bcast:15 row_mask:0xa bank_mask:0xf
	s_nop 1
	v_max_f32_dpp v41, v41, v41 row_bcast:31 row_mask:0xc bank_mask:0xf
	s_nop 1
	v_readlane_b32 s28, v41, 63
	s_nop 1
	v_div_scale_f32 v48, s[30:31], s28, s28, v47
	v_rcp_f32_e32 v49, v48
	s_nop 0
	v_fma_f32 v50, -v48, v49, 1.0
	v_fmac_f32_e32 v49, v50, v49
	v_mov_b32_e32 v50, s28
	v_div_scale_f32 v50, vcc, s32, v50, s32
	v_mul_f32_e32 v51, v50, v49
	v_fma_f32 v52, -v48, v51, v50
	v_fmac_f32_e32 v51, v52, v49
	v_fma_f32 v48, -v48, v51, v50
	v_div_fmas_f32 v48, v48, v49, v51
	v_div_fixup_f32 v48, v48, s28, v47
	v_cmp_gt_f32_e64 vcc, s28, 0
	v_writelane_b32 v40, s28, 8
	s_nop 0
	v_cndmask_b32_e32 v48, 0, v48, vcc
	v_fmaak_f32 v49, v18, v48, 0x4b400000
	v_fmaak_f32 v50, v19, v48, 0x4b400000
	v_fmaak_f32 v51, v20, v48, 0x4b400000
	v_fmaak_f32 v52, v21, v48, 0x4b400000
	v_perm_b32 v49, v50, v49, s33
	v_perm_b32 v51, v52, v51, s34
	v_or_b32_e32 v88, v49, v51
	v_fmaak_f32 v53, v22, v48, 0x4b400000
	v_fmaak_f32 v54, v23, v48, 0x4b400000
	v_fmaak_f32 v55, v24, v48, 0x4b400000
	v_fmaak_f32 v46, v25, v48, 0x4b400000
	v_perm_b32 v53, v54, v53, s33
	v_perm_b32 v55, v46, v55, s34
	v_or_b32_e32 v89, v53, v55
	v_fmaak_f32 v49, v26, v48, 0x4b400000
	v_fmaak_f32 v50, v27, v48, 0x4b400000
	v_fmaak_f32 v51, v28, v48, 0x4b400000
	v_fmaak_f32 v52, v29, v48, 0x4b400000
	v_perm_b32 v49, v50, v49, s33
	v_perm_b32 v51, v52, v51, s34
	v_or_b32_e32 v90, v49, v51
	v_fmaak_f32 v53, v30, v48, 0x4b400000
	v_fmaak_f32 v54, v31, v48, 0x4b400000
	v_fmaak_f32 v55, v32, v48, 0x4b400000
	v_fmaak_f32 v46, v33, v48, 0x4b400000
	v_perm_b32 v53, v54, v53, s33
	v_perm_b32 v55, v46, v55, s34
	v_or_b32_e32 v91, v53, v55
	s_waitcnt vmcnt(4)
	ds_read_b128 v[18:21], v38 offset:4096
	ds_read_b128 v[22:25], v38 offset:5120
	ds_read_b128 v[26:29], v38 offset:6144
	ds_read_b128 v[30:33], v38 offset:7168
	s_waitcnt lgkmcnt(0)
	s_mov_b32 m0, s36
	s_nop 0
	global_load_lds_dwordx4 v34, s[16:17] nt
	global_load_lds_dwordx4 v34, s[16:17] offset:1024 nt
	global_load_lds_dwordx4 v34, s[16:17] offset:2048 nt
	global_load_lds_dwordx4 v35, s[16:17] offset:3072 nt
	s_add_u32 s16, s16, 0x7d00
	s_addc_u32 s17, s17, 0
	v_cndmask_b32_e64 v30, 0, v30, s[18:19]
	v_cndmask_b32_e64 v31, 0, v31, s[18:19]
	v_cndmask_b32_e64 v32, 0, v32, s[18:19]
	v_cndmask_b32_e64 v33, 0, v33, s[18:19]
	v_max3_f32 v41, |v18|, |v19|, |v20|
	v_max3_f32 v42, |v21|, |v22|, |v23|
	v_max3_f32 v43, |v24|, |v25|, |v26|
	v_max3_f32 v44, |v27|, |v28|, |v29|
	v_max3_f32 v45, |v30|, |v31|, |v32|
	v_max3_f32 v41, v41, v42, |v33|
	v_max3_f32 v43, v43, v44, v45
	v_max_f32_e32 v41, v41, v43
	v_pk_add_f32 v[2:3], v[2:3], v[18:19]
	v_pk_add_f32 v[4:5], v[4:5], v[20:21]
	v_max_f32_dpp v41, v41, v41 quad_perm:[1,0,3,2] row_mask:0xf bank_mask:0xf
	v_pk_add_f32 v[6:7], v[6:7], v[22:23]
	v_pk_add_f32 v[8:9], v[8:9], v[24:25]
	v_max_f32_dpp v41, v41, v41 quad_perm:[2,3,0,1] row_mask:0xf bank_mask:0xf
	v_pk_add_f32 v[10:11], v[10:11], v[26:27]
	v_pk_add_f32 v[12:13], v[12:13], v[28:29]
	v_max_f32_dpp v41, v41, v41 row_half_mirror row_mask:0xf bank_mask:0xf
	v_pk_add_f32 v[14:15], v[14:15], v[30:31]
	v_pk_add_f32 v[16:17], v[16:17], v[32:33]
	v_max_f32_dpp v41, v41, v41 row_mirror row_mask:0xf bank_mask:0xf
	s_nop 1
	v_max_f32_dpp v41, v41, v41 row_bcast:15 row_mask:0xa bank_mask:0xf
	s_nop 1
	v_max_f32_dpp v41, v41, v41 row_bcast:31 row_mask:0xc bank_mask:0xf
	s_nop 1
	v_readlane_b32 s28, v41, 63
	s_nop 1
	v_div_scale_f32 v48, s[30:31], s28, s28, v47
	v_rcp_f32_e32 v49, v48
	s_nop 0
	v_fma_f32 v50, -v48, v49, 1.0
	v_fmac_f32_e32 v49, v50, v49
	v_mov_b32_e32 v50, s28
	v_div_scale_f32 v50, vcc, s32, v50, s32
	v_mul_f32_e32 v51, v50, v49
	v_fma_f32 v52, -v48, v51, v50
	v_fmac_f32_e32 v51, v52, v49
	v_fma_f32 v48, -v48, v51, v50
	v_div_fmas_f32 v48, v48, v49, v51
	v_div_fixup_f32 v48, v48, s28, v47
	v_cmp_gt_f32_e64 vcc, s28, 0
	v_writelane_b32 v40, s28, 9
	s_nop 0
	v_cndmask_b32_e32 v48, 0, v48, vcc
	v_fmaak_f32 v49, v18, v48, 0x4b400000
	v_fmaak_f32 v50, v19, v48, 0x4b400000
	v_fmaak_f32 v51, v20, v48, 0x4b400000
	v_fmaak_f32 v52, v21, v48, 0x4b400000
	v_perm_b32 v49, v50, v49, s33
	v_perm_b32 v51, v52, v51, s34
	v_or_b32_e32 v92, v49, v51
	v_fmaak_f32 v53, v22, v48, 0x4b400000
	v_fmaak_f32 v54, v23, v48, 0x4b400000
	v_fmaak_f32 v55, v24, v48, 0x4b400000
	v_fmaak_f32 v46, v25, v48, 0x4b400000
	v_perm_b32 v53, v54, v53, s33
	v_perm_b32 v55, v46, v55, s34
	v_or_b32_e32 v93, v53, v55
	v_fmaak_f32 v49, v26, v48, 0x4b400000
	v_fmaak_f32 v50, v27, v48, 0x4b400000
	v_fmaak_f32 v51, v28, v48, 0x4b400000
	v_fmaak_f32 v52, v29, v48, 0x4b400000
	v_perm_b32 v49, v50, v49, s33
	v_perm_b32 v51, v52, v51, s34
	v_or_b32_e32 v94, v49, v51
	v_fmaak_f32 v53, v30, v48, 0x4b400000
	v_fmaak_f32 v54, v31, v48, 0x4b400000
	v_fmaak_f32 v55, v32, v48, 0x4b400000
	v_fmaak_f32 v46, v33, v48, 0x4b400000
	v_perm_b32 v53, v54, v53, s33
	v_perm_b32 v55, v46, v55, s34
	v_or_b32_e32 v95, v53, v55
	s_waitcnt vmcnt(4)
	ds_read_b128 v[18:21], v38 offset:0
	ds_read_b128 v[22:25], v38 offset:1024
	ds_read_b128 v[26:29], v38 offset:2048
	ds_read_b128 v[30:33], v38 offset:3072
	s_waitcnt lgkmcnt(0)
	s_mov_b32 m0, s35
	s_nop 0
	global_load_lds_dwordx4 v34, s[16:17] nt
	global_load_lds_dwordx4 v34, s[16:17] offset:1024 nt
	global_load_lds_dwordx4 v34, s[16:17] offset:2048 nt
	global_load_lds_dwordx4 v35, s[16:17] offset:3072 nt
	s_add_u32 s16, s16, 0x7d00
	s_addc_u32 s17, s17, 0
	v_cndmask_b32_e64 v30, 0, v30, s[18:19]
	v_cndmask_b32_e64 v31, 0, v31, s[18:19]
	v_cndmask_b32_e64 v32, 0, v32, s[18:19]
	v_cndmask_b32_e64 v33, 0, v33, s[18:19]
	v_max3_f32 v41, |v18|, |v19|, |v20|
	v_max3_f32 v42, |v21|, |v22|, |v23|
	v_max3_f32 v43, |v24|, |v25|, |v26|
	v_max3_f32 v44, |v27|, |v28|, |v29|
	v_max3_f32 v45, |v30|, |v31|, |v32|
	v_max3_f32 v41, v41, v42, |v33|
	v_max3_f32 v43, v43, v44, v45
	v_max_f32_e32 v41, v41, v43
	v_pk_add_f32 v[2:3], v[2:3], v[18:19]
	v_pk_add_f32 v[4:5], v[4:5], v[20:21]
	v_max_f32_dpp v41, v41, v41 quad_perm:[1,0,3,2] row_mask:0xf bank_mask:0xf
	v_pk_add_f32 v[6:7], v[6:7], v[22:23]
	v_pk_add_f32 v[8:9], v[8:9], v[24:25]
	v_max_f32_dpp v41, v41, v41 quad_perm:[2,3,0,1] row_mask:0xf bank_mask:0xf
	v_pk_add_f32 v[10:11], v[10:11], v[26:27]
	v_pk_add_f32 v[12:13], v[12:13], v[28:29]
	v_max_f32_dpp v41, v41, v41 row_half_mirror row_mask:0xf bank_mask:0xf
	v_pk_add_f32 v[14:15], v[14:15], v[30:31]
	v_pk_add_f32 v[16:17], v[16:17], v[32:33]
	v_max_f32_dpp v41, v41, v41 row_mirror row_mask:0xf bank_mask:0xf
	s_nop 1
	v_max_f32_dpp v41, v41, v41 row_bcast:15 row_mask:0xa bank_mask:0xf
	s_nop 1
	v_max_f32_dpp v41, v41, v41 row_bcast:31 row_mask:0xc bank_mask:0xf
	s_nop 1
	v_readlane_b32 s28, v41, 63
	s_nop 1
	v_div_scale_f32 v48, s[30:31], s28, s28, v47
	v_rcp_f32_e32 v49, v48
	s_nop 0
	v_fma_f32 v50, -v48, v49, 1.0
	v_fmac_f32_e32 v49, v50, v49
	v_mov_b32_e32 v50, s28
	v_div_scale_f32 v50, vcc, s32, v50, s32
	v_mul_f32_e32 v51, v50, v49
	v_fma_f32 v52, -v48, v51, v50
	v_fmac_f32_e32 v51, v52, v49
	v_fma_f32 v48, -v48, v51, v50
	v_div_fmas_f32 v48, v48, v49, v51
	v_div_fixup_f32 v48, v48, s28, v47
	v_cmp_gt_f32_e64 vcc, s28, 0
	v_writelane_b32 v40, s28, 10
	s_nop 0
	v_cndmask_b32_e32 v48, 0, v48, vcc
	v_fmaak_f32 v49, v18, v48, 0x4b400000
	v_fmaak_f32 v50, v19, v48, 0x4b400000
	v_fmaak_f32 v51, v20, v48, 0x4b400000
	v_fmaak_f32 v52, v21, v48, 0x4b400000
	v_perm_b32 v49, v50, v49, s33
	v_perm_b32 v51, v52, v51, s34
	v_or_b32_e32 v96, v49, v51
	v_fmaak_f32 v53, v22, v48, 0x4b400000
	v_fmaak_f32 v54, v23, v48, 0x4b400000
	v_fmaak_f32 v55, v24, v48, 0x4b400000
	v_fmaak_f32 v46, v25, v48, 0x4b400000
	v_perm_b32 v53, v54, v53, s33
	v_perm_b32 v55, v46, v55, s34
	v_or_b32_e32 v97, v53, v55
	v_fmaak_f32 v49, v26, v48, 0x4b400000
	v_fmaak_f32 v50, v27, v48, 0x4b400000
	v_fmaak_f32 v51, v28, v48, 0x4b400000
	v_fmaak_f32 v52, v29, v48, 0x4b400000
	v_perm_b32 v49, v50, v49, s33
	v_perm_b32 v51, v52, v51, s34
	v_or_b32_e32 v98, v49, v51
	v_fmaak_f32 v53, v30, v48, 0x4b400000
	v_fmaak_f32 v54, v31, v48, 0x4b400000
	v_fmaak_f32 v55, v32, v48, 0x4b400000
	v_fmaak_f32 v46, v33, v48, 0x4b400000
	v_perm_b32 v53, v54, v53, s33
	v_perm_b32 v55, v46, v55, s34
	v_or_b32_e32 v99, v53, v55
	s_waitcnt vmcnt(4)
	ds_read_b128 v[18:21], v38 offset:4096
	ds_read_b128 v[22:25], v38 offset:5120
	ds_read_b128 v[26:29], v38 offset:6144
	ds_read_b128 v[30:33], v38 offset:7168
	s_waitcnt lgkmcnt(0)
	s_mov_b32 m0, s36
	s_nop 0
	global_load_lds_dwordx4 v34, s[16:17] nt
	global_load_lds_dwordx4 v34, s[16:17] offset:1024 nt
	global_load_lds_dwordx4 v34, s[16:17] offset:2048 nt
	global_load_lds_dwordx4 v35, s[16:17] offset:3072 nt
	s_add_u32 s16, s16, 0x7d00
	s_addc_u32 s17, s17, 0
	v_cndmask_b32_e64 v30, 0, v30, s[18:19]
	v_cndmask_b32_e64 v31, 0, v31, s[18:19]
	v_cndmask_b32_e64 v32, 0, v32, s[18:19]
	v_cndmask_b32_e64 v33, 0, v33, s[18:19]
	v_max3_f32 v41, |v18|, |v19|, |v20|
	v_max3_f32 v42, |v21|, |v22|, |v23|
	v_max3_f32 v43, |v24|, |v25|, |v26|
	v_max3_f32 v44, |v27|, |v28|, |v29|
	v_max3_f32 v45, |v30|, |v31|, |v32|
	v_max3_f32 v41, v41, v42, |v33|
	v_max3_f32 v43, v43, v44, v45
	v_max_f32_e32 v41, v41, v43
	v_pk_add_f32 v[2:3], v[2:3], v[18:19]
	v_pk_add_f32 v[4:5], v[4:5], v[20:21]
	v_max_f32_dpp v41, v41, v41 quad_perm:[1,0,3,2] row_mask:0xf bank_mask:0xf
	v_pk_add_f32 v[6:7], v[6:7], v[22:23]
	v_pk_add_f32 v[8:9], v[8:9], v[24:25]
	v_max_f32_dpp v41, v41, v41 quad_perm:[2,3,0,1] row_mask:0xf bank_mask:0xf
	v_pk_add_f32 v[10:11], v[10:11], v[26:27]
	v_pk_add_f32 v[12:13], v[12:13], v[28:29]
	v_max_f32_dpp v41, v41, v41 row_half_mirror row_mask:0xf bank_mask:0xf
	v_pk_add_f32 v[14:15], v[14:15], v[30:31]
	v_pk_add_f32 v[16:17], v[16:17], v[32:33]
	v_max_f32_dpp v41, v41, v41 row_mirror row_mask:0xf bank_mask:0xf
	s_nop 1
	v_max_f32_dpp v41, v41, v41 row_bcast:15 row_mask:0xa bank_mask:0xf
	s_nop 1
	v_max_f32_dpp v41, v41, v41 row_bcast:31 row_mask:0xc bank_mask:0xf
	s_nop 1
	v_readlane_b32 s28, v41, 63
	s_nop 1
	v_div_scale_f32 v48, s[30:31], s28, s28, v47
	v_rcp_f32_e32 v49, v48
	s_nop 0
	v_fma_f32 v50, -v48, v49, 1.0
	v_fmac_f32_e32 v49, v50, v49
	v_mov_b32_e32 v50, s28
	v_div_scale_f32 v50, vcc, s32, v50, s32
	v_mul_f32_e32 v51, v50, v49
	v_fma_f32 v52, -v48, v51, v50
	v_fmac_f32_e32 v51, v52, v49
	v_fma_f32 v48, -v48, v51, v50
	v_div_fmas_f32 v48, v48, v49, v51
	v_div_fixup_f32 v48, v48, s28, v47
	v_cmp_gt_f32_e64 vcc, s28, 0
	v_writelane_b32 v40, s28, 11
	s_nop 0
	v_cndmask_b32_e32 v48, 0, v48, vcc
	v_fmaak_f32 v49, v18, v48, 0x4b400000
	v_fmaak_f32 v50, v19, v48, 0x4b400000
	v_fmaak_f32 v51, v20, v48, 0x4b400000
	v_fmaak_f32 v52, v21, v48, 0x4b400000
	v_perm_b32 v49, v50, v49, s33
	v_perm_b32 v51, v52, v51, s34
	v_or_b32_e32 v100, v49, v51
	v_fmaak_f32 v53, v22, v48, 0x4b400000
	v_fmaak_f32 v54, v23, v48, 0x4b400000
	v_fmaak_f32 v55, v24, v48, 0x4b400000
	v_fmaak_f32 v46, v25, v48, 0x4b400000
	v_perm_b32 v53, v54, v53, s33
	v_perm_b32 v55, v46, v55, s34
	v_or_b32_e32 v101, v53, v55
	v_fmaak_f32 v49, v26, v48, 0x4b400000
	v_fmaak_f32 v50, v27, v48, 0x4b400000
	v_fmaak_f32 v51, v28, v48, 0x4b400000
	v_fmaak_f32 v52, v29, v48, 0x4b400000
	v_perm_b32 v49, v50, v49, s33
	v_perm_b32 v51, v52, v51, s34
	v_or_b32_e32 v102, v49, v51
	v_fmaak_f32 v53, v30, v48, 0x4b400000
	v_fmaak_f32 v54, v31, v48, 0x4b400000
	v_fmaak_f32 v55, v32, v48, 0x4b400000
	v_fmaak_f32 v46, v33, v48, 0x4b400000
	v_perm_b32 v53, v54, v53, s33
	v_perm_b32 v55, v46, v55, s34
	v_or_b32_e32 v103, v53, v55
	s_waitcnt vmcnt(4)
	ds_read_b128 v[18:21], v38 offset:0
	ds_read_b128 v[22:25], v38 offset:1024
	ds_read_b128 v[26:29], v38 offset:2048
	ds_read_b128 v[30:33], v38 offset:3072
	s_waitcnt lgkmcnt(0)
	s_mov_b32 m0, s35
	s_nop 0
	global_load_lds_dwordx4 v34, s[16:17] nt
	global_load_lds_dwordx4 v34, s[16:17] offset:1024 nt
	global_load_lds_dwordx4 v34, s[16:17] offset:2048 nt
	global_load_lds_dwordx4 v35, s[16:17] offset:3072 nt
	s_add_u32 s16, s16, 0x7d00
	s_addc_u32 s17, s17, 0
	v_cndmask_b32_e64 v30, 0, v30, s[18:19]
	v_cndmask_b32_e64 v31, 0, v31, s[18:19]
	v_cndmask_b32_e64 v32, 0, v32, s[18:19]
	v_cndmask_b32_e64 v33, 0, v33, s[18:19]
	v_max3_f32 v41, |v18|, |v19|, |v20|
	v_max3_f32 v42, |v21|, |v22|, |v23|
	v_max3_f32 v43, |v24|, |v25|, |v26|
	v_max3_f32 v44, |v27|, |v28|, |v29|
	v_max3_f32 v45, |v30|, |v31|, |v32|
	v_max3_f32 v41, v41, v42, |v33|
	v_max3_f32 v43, v43, v44, v45
	v_max_f32_e32 v41, v41, v43
	v_pk_add_f32 v[2:3], v[2:3], v[18:19]
	v_pk_add_f32 v[4:5], v[4:5], v[20:21]
	v_max_f32_dpp v41, v41, v41 quad_perm:[1,0,3,2] row_mask:0xf bank_mask:0xf
	v_pk_add_f32 v[6:7], v[6:7], v[22:23]
	v_pk_add_f32 v[8:9], v[8:9], v[24:25]
	v_max_f32_dpp v41, v41, v41 quad_perm:[2,3,0,1] row_mask:0xf bank_mask:0xf
	v_pk_add_f32 v[10:11], v[10:11], v[26:27]
	v_pk_add_f32 v[12:13], v[12:13], v[28:29]
	v_max_f32_dpp v41, v41, v41 row_half_mirror row_mask:0xf bank_mask:0xf
	v_pk_add_f32 v[14:15], v[14:15], v[30:31]
	v_pk_add_f32 v[16:17], v[16:17], v[32:33]
	v_max_f32_dpp v41, v41, v41 row_mirror row_mask:0xf bank_mask:0xf
	s_nop 1
	v_max_f32_dpp v41, v41, v41 row_bcast:15 row_mask:0xa bank_mask:0xf
	s_nop 1
	v_max_f32_dpp v41, v41, v41 row_bcast:31 row_mask:0xc bank_mask:0xf
	s_nop 1
	v_readlane_b32 s28, v41, 63
	s_nop 1
	v_div_scale_f32 v48, s[30:31], s28, s28, v47
	v_rcp_f32_e32 v49, v48
	s_nop 0
	v_fma_f32 v50, -v48, v49, 1.0
	v_fmac_f32_e32 v49, v50, v49
	v_mov_b32_e32 v50, s28
	v_div_scale_f32 v50, vcc, s32, v50, s32
	v_mul_f32_e32 v51, v50, v49
	v_fma_f32 v52, -v48, v51, v50
	v_fmac_f32_e32 v51, v52, v49
	v_fma_f32 v48, -v48, v51, v50
	v_div_fmas_f32 v48, v48, v49, v51
	v_div_fixup_f32 v48, v48, s28, v47
	v_cmp_gt_f32_e64 vcc, s28, 0
	v_writelane_b32 v40, s28, 12
	s_nop 0
	v_cndmask_b32_e32 v48, 0, v48, vcc
	v_fmaak_f32 v49, v18, v48, 0x4b400000
	v_fmaak_f32 v50, v19, v48, 0x4b400000
	v_fmaak_f32 v51, v20, v48, 0x4b400000
	v_fmaak_f32 v52, v21, v48, 0x4b400000
	v_perm_b32 v49, v50, v49, s33
	v_perm_b32 v51, v52, v51, s34
	v_or_b32_e32 v104, v49, v51
	v_fmaak_f32 v53, v22, v48, 0x4b400000
	v_fmaak_f32 v54, v23, v48, 0x4b400000
	v_fmaak_f32 v55, v24, v48, 0x4b400000
	v_fmaak_f32 v46, v25, v48, 0x4b400000
	v_perm_b32 v53, v54, v53, s33
	v_perm_b32 v55, v46, v55, s34
	v_or_b32_e32 v105, v53, v55
	v_fmaak_f32 v49, v26, v48, 0x4b400000
	v_fmaak_f32 v50, v27, v48, 0x4b400000
	v_fmaak_f32 v51, v28, v48, 0x4b400000
	v_fmaak_f32 v52, v29, v48, 0x4b400000
	v_perm_b32 v49, v50, v49, s33
	v_perm_b32 v51, v52, v51, s34
	v_or_b32_e32 v106, v49, v51
	v_fmaak_f32 v53, v30, v48, 0x4b400000
	v_fmaak_f32 v54, v31, v48, 0x4b400000
	v_fmaak_f32 v55, v32, v48, 0x4b400000
	v_fmaak_f32 v46, v33, v48, 0x4b400000
	v_perm_b32 v53, v54, v53, s33
	v_perm_b32 v55, v46, v55, s34
	v_or_b32_e32 v107, v53, v55
	s_waitcnt vmcnt(4)
	ds_read_b128 v[18:21], v38 offset:4096
	ds_read_b128 v[22:25], v38 offset:5120
	ds_read_b128 v[26:29], v38 offset:6144
	ds_read_b128 v[30:33], v38 offset:7168
	s_waitcnt lgkmcnt(0)
	s_mov_b32 m0, s36
	s_nop 0
	global_load_lds_dwordx4 v34, s[16:17] nt
	global_load_lds_dwordx4 v34, s[16:17] offset:1024 nt
	global_load_lds_dwordx4 v34, s[16:17] offset:2048 nt
	global_load_lds_dwordx4 v35, s[16:17] offset:3072 nt
	s_add_u32 s16, s16, 0x7d00
	s_addc_u32 s17, s17, 0
	v_cndmask_b32_e64 v30, 0, v30, s[18:19]
	v_cndmask_b32_e64 v31, 0, v31, s[18:19]
	v_cndmask_b32_e64 v32, 0, v32, s[18:19]
	v_cndmask_b32_e64 v33, 0, v33, s[18:19]
	v_max3_f32 v41, |v18|, |v19|, |v20|
	v_max3_f32 v42, |v21|, |v22|, |v23|
	v_max3_f32 v43, |v24|, |v25|, |v26|
	v_max3_f32 v44, |v27|, |v28|, |v29|
	v_max3_f32 v45, |v30|, |v31|, |v32|
	v_max3_f32 v41, v41, v42, |v33|
	v_max3_f32 v43, v43, v44, v45
	v_max_f32_e32 v41, v41, v43
	v_pk_add_f32 v[2:3], v[2:3], v[18:19]
	v_pk_add_f32 v[4:5], v[4:5], v[20:21]
	v_max_f32_dpp v41, v41, v41 quad_perm:[1,0,3,2] row_mask:0xf bank_mask:0xf
	v_pk_add_f32 v[6:7], v[6:7], v[22:23]
	v_pk_add_f32 v[8:9], v[8:9], v[24:25]
	v_max_f32_dpp v41, v41, v41 quad_perm:[2,3,0,1] row_mask:0xf bank_mask:0xf
	v_pk_add_f32 v[10:11], v[10:11], v[26:27]
	v_pk_add_f32 v[12:13], v[12:13], v[28:29]
	v_max_f32_dpp v41, v41, v41 row_half_mirror row_mask:0xf bank_mask:0xf
	v_pk_add_f32 v[14:15], v[14:15], v[30:31]
	v_pk_add_f32 v[16:17], v[16:17], v[32:33]
	v_max_f32_dpp v41, v41, v41 row_mirror row_mask:0xf bank_mask:0xf
	s_nop 1
	v_max_f32_dpp v41, v41, v41 row_bcast:15 row_mask:0xa bank_mask:0xf
	s_nop 1
	v_max_f32_dpp v41, v41, v41 row_bcast:31 row_mask:0xc bank_mask:0xf
	s_nop 1
	v_readlane_b32 s28, v41, 63
	s_nop 1
	v_div_scale_f32 v48, s[30:31], s28, s28, v47
	v_rcp_f32_e32 v49, v48
	s_nop 0
	v_fma_f32 v50, -v48, v49, 1.0
	v_fmac_f32_e32 v49, v50, v49
	v_mov_b32_e32 v50, s28
	v_div_scale_f32 v50, vcc, s32, v50, s32
	v_mul_f32_e32 v51, v50, v49
	v_fma_f32 v52, -v48, v51, v50
	v_fmac_f32_e32 v51, v52, v49
	v_fma_f32 v48, -v48, v51, v50
	v_div_fmas_f32 v48, v48, v49, v51
	v_div_fixup_f32 v48, v48, s28, v47
	v_cmp_gt_f32_e64 vcc, s28, 0
	v_writelane_b32 v40, s28, 13
	s_nop 0
	v_cndmask_b32_e32 v48, 0, v48, vcc
	v_fmaak_f32 v49, v18, v48, 0x4b400000
	v_fmaak_f32 v50, v19, v48, 0x4b400000
	v_fmaak_f32 v51, v20, v48, 0x4b400000
	v_fmaak_f32 v52, v21, v48, 0x4b400000
	v_perm_b32 v49, v50, v49, s33
	v_perm_b32 v51, v52, v51, s34
	v_or_b32_e32 v108, v49, v51
	v_fmaak_f32 v53, v22, v48, 0x4b400000
	v_fmaak_f32 v54, v23, v48, 0x4b400000
	v_fmaak_f32 v55, v24, v48, 0x4b400000
	v_fmaak_f32 v46, v25, v48, 0x4b400000
	v_perm_b32 v53, v54, v53, s33
	v_perm_b32 v55, v46, v55, s34
	v_or_b32_e32 v109, v53, v55
	v_fmaak_f32 v49, v26, v48, 0x4b400000
	v_fmaak_f32 v50, v27, v48, 0x4b400000
	v_fmaak_f32 v51, v28, v48, 0x4b400000
	v_fmaak_f32 v52, v29, v48, 0x4b400000
	v_perm_b32 v49, v50, v49, s33
	v_perm_b32 v51, v52, v51, s34
	v_or_b32_e32 v110, v49, v51
	v_fmaak_f32 v53, v30, v48, 0x4b400000
	v_fmaak_f32 v54, v31, v48, 0x4b400000
	v_fmaak_f32 v55, v32, v48, 0x4b400000
	v_fmaak_f32 v46, v33, v48, 0x4b400000
	v_perm_b32 v53, v54, v53, s33
	v_perm_b32 v55, v46, v55, s34
	v_or_b32_e32 v111, v53, v55
	s_waitcnt vmcnt(4)
	ds_read_b128 v[18:21], v38 offset:0
	ds_read_b128 v[22:25], v38 offset:1024
	ds_read_b128 v[26:29], v38 offset:2048
	ds_read_b128 v[30:33], v38 offset:3072
	s_waitcnt lgkmcnt(0)
	s_mov_b32 m0, s35
	s_nop 0
	global_load_lds_dwordx4 v34, s[16:17] nt
	global_load_lds_dwordx4 v34, s[16:17] offset:1024 nt
	global_load_lds_dwordx4 v34, s[16:17] offset:2048 nt
	global_load_lds_dwordx4 v35, s[16:17] offset:3072 nt
	s_add_u32 s16, s16, 0x7d00
	s_addc_u32 s17, s17, 0
	v_cndmask_b32_e64 v30, 0, v30, s[18:19]
	v_cndmask_b32_e64 v31, 0, v31, s[18:19]
	v_cndmask_b32_e64 v32, 0, v32, s[18:19]
	v_cndmask_b32_e64 v33, 0, v33, s[18:19]
	v_max3_f32 v41, |v18|, |v19|, |v20|
	v_max3_f32 v42, |v21|, |v22|, |v23|
	v_max3_f32 v43, |v24|, |v25|, |v26|
	v_max3_f32 v44, |v27|, |v28|, |v29|
	v_max3_f32 v45, |v30|, |v31|, |v32|
	v_max3_f32 v41, v41, v42, |v33|
	v_max3_f32 v43, v43, v44, v45
	v_max_f32_e32 v41, v41, v43
	v_pk_add_f32 v[2:3], v[2:3], v[18:19]
	v_pk_add_f32 v[4:5], v[4:5], v[20:21]
	v_max_f32_dpp v41, v41, v41 quad_perm:[1,0,3,2] row_mask:0xf bank_mask:0xf
	v_pk_add_f32 v[6:7], v[6:7], v[22:23]
	v_pk_add_f32 v[8:9], v[8:9], v[24:25]
	v_max_f32_dpp v41, v41, v41 quad_perm:[2,3,0,1] row_mask:0xf bank_mask:0xf
	v_pk_add_f32 v[10:11], v[10:11], v[26:27]
	v_pk_add_f32 v[12:13], v[12:13], v[28:29]
	v_max_f32_dpp v41, v41, v41 row_half_mirror row_mask:0xf bank_mask:0xf
	v_pk_add_f32 v[14:15], v[14:15], v[30:31]
	v_pk_add_f32 v[16:17], v[16:17], v[32:33]
	v_max_f32_dpp v41, v41, v41 row_mirror row_mask:0xf bank_mask:0xf
	s_nop 1
	v_max_f32_dpp v41, v41, v41 row_bcast:15 row_mask:0xa bank_mask:0xf
	s_nop 1
	v_max_f32_dpp v41, v41, v41 row_bcast:31 row_mask:0xc bank_mask:0xf
	s_nop 1
	v_readlane_b32 s28, v41, 63
	s_nop 1
	v_div_scale_f32 v48, s[30:31], s28, s28, v47
	v_rcp_f32_e32 v49, v48
	s_nop 0
	v_fma_f32 v50, -v48, v49, 1.0
	v_fmac_f32_e32 v49, v50, v49
	v_mov_b32_e32 v50, s28
	v_div_scale_f32 v50, vcc, s32, v50, s32
	v_mul_f32_e32 v51, v50, v49
	v_fma_f32 v52, -v48, v51, v50
	v_fmac_f32_e32 v51, v52, v49
	v_fma_f32 v48, -v48, v51, v50
	v_div_fmas_f32 v48, v48, v49, v51
	v_div_fixup_f32 v48, v48, s28, v47
	v_cmp_gt_f32_e64 vcc, s28, 0
	v_writelane_b32 v40, s28, 14
	s_nop 0
	v_cndmask_b32_e32 v48, 0, v48, vcc
	v_fmaak_f32 v49, v18, v48, 0x4b400000
	v_fmaak_f32 v50, v19, v48, 0x4b400000
	v_fmaak_f32 v51, v20, v48, 0x4b400000
	v_fmaak_f32 v52, v21, v48, 0x4b400000
	v_perm_b32 v49, v50, v49, s33
	v_perm_b32 v51, v52, v51, s34
	v_or_b32_e32 v112, v49, v51
	v_fmaak_f32 v53, v22, v48, 0x4b400000
	v_fmaak_f32 v54, v23, v48, 0x4b400000
	v_fmaak_f32 v55, v24, v48, 0x4b400000
	v_fmaak_f32 v46, v25, v48, 0x4b400000
	v_perm_b32 v53, v54, v53, s33
	v_perm_b32 v55, v46, v55, s34
	v_or_b32_e32 v113, v53, v55
	v_fmaak_f32 v49, v26, v48, 0x4b400000
	v_fmaak_f32 v50, v27, v48, 0x4b400000
	v_fmaak_f32 v51, v28, v48, 0x4b400000
	v_fmaak_f32 v52, v29, v48, 0x4b400000
	v_perm_b32 v49, v50, v49, s33
	v_perm_b32 v51, v52, v51, s34
	v_or_b32_e32 v114, v49, v51
	v_fmaak_f32 v53, v30, v48, 0x4b400000
	v_fmaak_f32 v54, v31, v48, 0x4b400000
	v_fmaak_f32 v55, v32, v48, 0x4b400000
	v_fmaak_f32 v46, v33, v48, 0x4b400000
	v_perm_b32 v53, v54, v53, s33
	v_perm_b32 v55, v46, v55, s34
	v_or_b32_e32 v115, v53, v55
	s_waitcnt vmcnt(4)
	ds_read_b128 v[18:21], v38 offset:4096
	ds_read_b128 v[22:25], v38 offset:5120
	ds_read_b128 v[26:29], v38 offset:6144
	ds_read_b128 v[30:33], v38 offset:7168
	s_waitcnt lgkmcnt(0)
	s_mov_b32 m0, s36
	s_nop 0
	global_load_lds_dwordx4 v34, s[16:17] nt
	global_load_lds_dwordx4 v34, s[16:17] offset:1024 nt
	global_load_lds_dwordx4 v34, s[16:17] offset:2048 nt
	global_load_lds_dwordx4 v35, s[16:17] offset:3072 nt
	s_add_u32 s16, s16, 0x7d00
	s_addc_u32 s17, s17, 0
	v_cndmask_b32_e64 v30, 0, v30, s[18:19]
	v_cndmask_b32_e64 v31, 0, v31, s[18:19]
	v_cndmask_b32_e64 v32, 0, v32, s[18:19]
	v_cndmask_b32_e64 v33, 0, v33, s[18:19]
	v_max3_f32 v41, |v18|, |v19|, |v20|
	v_max3_f32 v42, |v21|, |v22|, |v23|
	v_max3_f32 v43, |v24|, |v25|, |v26|
	v_max3_f32 v44, |v27|, |v28|, |v29|
	v_max3_f32 v45, |v30|, |v31|, |v32|
	v_max3_f32 v41, v41, v42, |v33|
	v_max3_f32 v43, v43, v44, v45
	v_max_f32_e32 v41, v41, v43
	v_pk_add_f32 v[2:3], v[2:3], v[18:19]
	v_pk_add_f32 v[4:5], v[4:5], v[20:21]
	v_max_f32_dpp v41, v41, v41 quad_perm:[1,0,3,2] row_mask:0xf bank_mask:0xf
	v_pk_add_f32 v[6:7], v[6:7], v[22:23]
	v_pk_add_f32 v[8:9], v[8:9], v[24:25]
	v_max_f32_dpp v41, v41, v41 quad_perm:[2,3,0,1] row_mask:0xf bank_mask:0xf
	v_pk_add_f32 v[10:11], v[10:11], v[26:27]
	v_pk_add_f32 v[12:13], v[12:13], v[28:29]
	v_max_f32_dpp v41, v41, v41 row_half_mirror row_mask:0xf bank_mask:0xf
	v_pk_add_f32 v[14:15], v[14:15], v[30:31]
	v_pk_add_f32 v[16:17], v[16:17], v[32:33]
	v_max_f32_dpp v41, v41, v41 row_mirror row_mask:0xf bank_mask:0xf
	s_nop 1
	v_max_f32_dpp v41, v41, v41 row_bcast:15 row_mask:0xa bank_mask:0xf
	s_nop 1
	v_max_f32_dpp v41, v41, v41 row_bcast:31 row_mask:0xc bank_mask:0xf
	s_nop 1
	v_readlane_b32 s28, v41, 63
	s_nop 1
	v_div_scale_f32 v48, s[30:31], s28, s28, v47
	v_rcp_f32_e32 v49, v48
	s_nop 0
	v_fma_f32 v50, -v48, v49, 1.0
	v_fmac_f32_e32 v49, v50, v49
	v_mov_b32_e32 v50, s28
	v_div_scale_f32 v50, vcc, s32, v50, s32
	v_mul_f32_e32 v51, v50, v49
	v_fma_f32 v52, -v48, v51, v50
	v_fmac_f32_e32 v51, v52, v49
	v_fma_f32 v48, -v48, v51, v50
	v_div_fmas_f32 v48, v48, v49, v51
	v_div_fixup_f32 v48, v48, s28, v47
	v_cmp_gt_f32_e64 vcc, s28, 0
	v_writelane_b32 v40, s28, 15
	s_nop 0
	v_cndmask_b32_e32 v48, 0, v48, vcc
	v_fmaak_f32 v49, v18, v48, 0x4b400000
	v_fmaak_f32 v50, v19, v48, 0x4b400000
	v_fmaak_f32 v51, v20, v48, 0x4b400000
	v_fmaak_f32 v52, v21, v48, 0x4b400000
	v_perm_b32 v49, v50, v49, s33
	v_perm_b32 v51, v52, v51, s34
	v_or_b32_e32 v49, v49, v51
	global_store_dword v39, v49, s[20:21]
	v_fmaak_f32 v53, v22, v48, 0x4b400000
	v_fmaak_f32 v54, v23, v48, 0x4b400000
	v_fmaak_f32 v55, v24, v48, 0x4b400000
	v_fmaak_f32 v46, v25, v48, 0x4b400000
	v_perm_b32 v53, v54, v53, s33
	v_perm_b32 v55, v46, v55, s34
	v_or_b32_e32 v53, v53, v55
	global_store_dword v39, v53, s[22:23]
	v_fmaak_f32 v49, v26, v48, 0x4b400000
	v_fmaak_f32 v50, v27, v48, 0x4b400000
	v_fmaak_f32 v51, v28, v48, 0x4b400000
	v_fmaak_f32 v52, v29, v48, 0x4b400000
	v_perm_b32 v49, v50, v49, s33
	v_perm_b32 v51, v52, v51, s34
	v_or_b32_e32 v49, v49, v51
	global_store_dword v39, v49, s[24:25]
	v_fmaak_f32 v53, v30, v48, 0x4b400000
	v_fmaak_f32 v54, v31, v48, 0x4b400000
	v_fmaak_f32 v55, v32, v48, 0x4b400000
	v_fmaak_f32 v46, v33, v48, 0x4b400000
	v_perm_b32 v53, v54, v53, s33
	v_perm_b32 v55, v46, v55, s34
	v_or_b32_e32 v53, v53, v55
	global_store_dword v39, v53, s[26:27]
	s_add_u32 s20, s20, 0x400
	s_addc_u32 s21, s21, 0
	s_add_u32 s22, s22, 0x400
	s_addc_u32 s23, s23, 0
	s_add_u32 s24, s24, 0x400
	s_addc_u32 s25, s25, 0
	s_add_u32 s26, s26, 0x400
	s_addc_u32 s27, s27, 0
	s_waitcnt vmcnt(8)
	ds_read_b128 v[18:21], v38 offset:0
	ds_read_b128 v[22:25], v38 offset:1024
	ds_read_b128 v[26:29], v38 offset:2048
	ds_read_b128 v[30:33], v38 offset:3072
	s_waitcnt lgkmcnt(0)
	s_mov_b32 m0, s35
	s_nop 0
	global_load_lds_dwordx4 v34, s[16:17] nt
	global_load_lds_dwordx4 v34, s[16:17] offset:1024 nt
	global_load_lds_dwordx4 v34, s[16:17] offset:2048 nt
	global_load_lds_dwordx4 v35, s[16:17] offset:3072 nt
	s_add_u32 s16, s16, 0x7d00
	s_addc_u32 s17, s17, 0
	v_cndmask_b32_e64 v30, 0, v30, s[18:19]
	v_cndmask_b32_e64 v31, 0, v31, s[18:19]
	v_cndmask_b32_e64 v32, 0, v32, s[18:19]
	v_cndmask_b32_e64 v33, 0, v33, s[18:19]
	v_max3_f32 v41, |v18|, |v19|, |v20|
	v_max3_f32 v42, |v21|, |v22|, |v23|
	v_max3_f32 v43, |v24|, |v25|, |v26|
	v_max3_f32 v44, |v27|, |v28|, |v29|
	v_max3_f32 v45, |v30|, |v31|, |v32|
	v_max3_f32 v41, v41, v42, |v33|
	v_max3_f32 v43, v43, v44, v45
	v_max_f32_e32 v41, v41, v43
	v_pk_add_f32 v[2:3], v[2:3], v[18:19]
	v_pk_add_f32 v[4:5], v[4:5], v[20:21]
	v_max_f32_dpp v41, v41, v41 quad_perm:[1,0,3,2] row_mask:0xf bank_mask:0xf
	v_pk_add_f32 v[6:7], v[6:7], v[22:23]
	v_pk_add_f32 v[8:9], v[8:9], v[24:25]
	v_max_f32_dpp v41, v41, v41 quad_perm:[2,3,0,1] row_mask:0xf bank_mask:0xf
	v_pk_add_f32 v[10:11], v[10:11], v[26:27]
	v_pk_add_f32 v[12:13], v[12:13], v[28:29]
	v_max_f32_dpp v41, v41, v41 row_half_mirror row_mask:0xf bank_mask:0xf
	v_pk_add_f32 v[14:15], v[14:15], v[30:31]
	v_pk_add_f32 v[16:17], v[16:17], v[32:33]
	v_max_f32_dpp v41, v41, v41 row_mirror row_mask:0xf bank_mask:0xf
	s_nop 1
	v_max_f32_dpp v41, v41, v41 row_bcast:15 row_mask:0xa bank_mask:0xf
	s_nop 1
	v_max_f32_dpp v41, v41, v41 row_bcast:31 row_mask:0xc bank_mask:0xf
	s_nop 1
	v_readlane_b32 s28, v41, 63
	s_nop 1
	v_div_scale_f32 v48, s[30:31], s28, s28, v47
	v_rcp_f32_e32 v49, v48
	s_nop 0
	v_fma_f32 v50, -v48, v49, 1.0
	v_fmac_f32_e32 v49, v50, v49
	v_mov_b32_e32 v50, s28
	v_div_scale_f32 v50, vcc, s32, v50, s32
	v_mul_f32_e32 v51, v50, v49
	v_fma_f32 v52, -v48, v51, v50
	v_fmac_f32_e32 v51, v52, v49
	v_fma_f32 v48, -v48, v51, v50
	v_div_fmas_f32 v48, v48, v49, v51
	v_div_fixup_f32 v48, v48, s28, v47
	v_cmp_gt_f32_e64 vcc, s28, 0
	v_writelane_b32 v40, s28, 16
	s_nop 0
	v_cndmask_b32_e32 v48, 0, v48, vcc
	v_fmaak_f32 v49, v18, v48, 0x4b400000
	v_fmaak_f32 v50, v19, v48, 0x4b400000
	v_fmaak_f32 v51, v20, v48, 0x4b400000
	v_fmaak_f32 v52, v21, v48, 0x4b400000
	v_perm_b32 v49, v50, v49, s33
	v_perm_b32 v51, v52, v51, s34
	v_or_b32_e32 v49, v49, v51
	global_store_dword v39, v49, s[20:21]
	v_fmaak_f32 v53, v22, v48, 0x4b400000
	v_fmaak_f32 v54, v23, v48, 0x4b400000
	v_fmaak_f32 v55, v24, v48, 0x4b400000
	v_fmaak_f32 v46, v25, v48, 0x4b400000
	v_perm_b32 v53, v54, v53, s33
	v_perm_b32 v55, v46, v55, s34
	v_or_b32_e32 v53, v53, v55
	global_store_dword v39, v53, s[22:23]
	v_fmaak_f32 v49, v26, v48, 0x4b400000
	v_fmaak_f32 v50, v27, v48, 0x4b400000
	v_fmaak_f32 v51, v28, v48, 0x4b400000
	v_fmaak_f32 v52, v29, v48, 0x4b400000
	v_perm_b32 v49, v50, v49, s33
	v_perm_b32 v51, v52, v51, s34
	v_or_b32_e32 v49, v49, v51
	global_store_dword v39, v49, s[24:25]
	v_fmaak_f32 v53, v30, v48, 0x4b400000
	v_fmaak_f32 v54, v31, v48, 0x4b400000
	v_fmaak_f32 v55, v32, v48, 0x4b400000
	v_fmaak_f32 v46, v33, v48, 0x4b400000
	v_perm_b32 v53, v54, v53, s33
	v_perm_b32 v55, v46, v55, s34
	v_or_b32_e32 v53, v53, v55
	global_store_dword v39, v53, s[26:27]
	s_add_u32 s20, s20, 0x400
	s_addc_u32 s21, s21, 0
	s_add_u32 s22, s22, 0x400
	s_addc_u32 s23, s23, 0
	s_add_u32 s24, s24, 0x400
	s_addc_u32 s25, s25, 0
	s_add_u32 s26, s26, 0x400
	s_addc_u32 s27, s27, 0
	s_waitcnt vmcnt(12)
	ds_read_b128 v[18:21], v38 offset:4096
	ds_read_b128 v[22:25], v38 offset:5120
	ds_read_b128 v[26:29], v38 offset:6144
	ds_read_b128 v[30:33], v38 offset:7168
	s_waitcnt lgkmcnt(0)
	s_mov_b32 m0, s36
	s_nop 0
	global_load_lds_dwordx4 v34, s[16:17] nt
	global_load_lds_dwordx4 v34, s[16:17] offset:1024 nt
	global_load_lds_dwordx4 v34, s[16:17] offset:2048 nt
	global_load_lds_dwordx4 v35, s[16:17] offset:3072 nt
	s_add_u32 s16, s16, 0x7d00
	s_addc_u32 s17, s17, 0
	v_cndmask_b32_e64 v30, 0, v30, s[18:19]
	v_cndmask_b32_e64 v31, 0, v31, s[18:19]
	v_cndmask_b32_e64 v32, 0, v32, s[18:19]
	v_cndmask_b32_e64 v33, 0, v33, s[18:19]
	v_max3_f32 v41, |v18|, |v19|, |v20|
	v_max3_f32 v42, |v21|, |v22|, |v23|
	v_max3_f32 v43, |v24|, |v25|, |v26|
	v_max3_f32 v44, |v27|, |v28|, |v29|
	v_max3_f32 v45, |v30|, |v31|, |v32|
	v_max3_f32 v41, v41, v42, |v33|
	v_max3_f32 v43, v43, v44, v45
	v_max_f32_e32 v41, v41, v43
	v_pk_add_f32 v[2:3], v[2:3], v[18:19]
	v_pk_add_f32 v[4:5], v[4:5], v[20:21]
	v_max_f32_dpp v41, v41, v41 quad_perm:[1,0,3,2] row_mask:0xf bank_mask:0xf
	v_pk_add_f32 v[6:7], v[6:7], v[22:23]
	v_pk_add_f32 v[8:9], v[8:9], v[24:25]
	v_max_f32_dpp v41, v41, v41 quad_perm:[2,3,0,1] row_mask:0xf bank_mask:0xf
	v_pk_add_f32 v[10:11], v[10:11], v[26:27]
	v_pk_add_f32 v[12:13], v[12:13], v[28:29]
	v_max_f32_dpp v41, v41, v41 row_half_mirror row_mask:0xf bank_mask:0xf
	v_pk_add_f32 v[14:15], v[14:15], v[30:31]
	v_pk_add_f32 v[16:17], v[16:17], v[32:33]
	v_max_f32_dpp v41, v41, v41 row_mirror row_mask:0xf bank_mask:0xf
	s_nop 1
	v_max_f32_dpp v41, v41, v41 row_bcast:15 row_mask:0xa bank_mask:0xf
	s_nop 1
	v_max_f32_dpp v41, v41, v41 row_bcast:31 row_mask:0xc bank_mask:0xf
	s_nop 1
	v_readlane_b32 s28, v41, 63
	s_nop 1
	v_div_scale_f32 v48, s[30:31], s28, s28, v47
	v_rcp_f32_e32 v49, v48
	s_nop 0
	v_fma_f32 v50, -v48, v49, 1.0
	v_fmac_f32_e32 v49, v50, v49
	v_mov_b32_e32 v50, s28
	v_div_scale_f32 v50, vcc, s32, v50, s32
	v_mul_f32_e32 v51, v50, v49
	v_fma_f32 v52, -v48, v51, v50
	v_fmac_f32_e32 v51, v52, v49
	v_fma_f32 v48, -v48, v51, v50
	v_div_fmas_f32 v48, v48, v49, v51
	v_div_fixup_f32 v48, v48, s28, v47
	v_cmp_gt_f32_e64 vcc, s28, 0
	v_writelane_b32 v40, s28, 17
	s_nop 0
	v_cndmask_b32_e32 v48, 0, v48, vcc
	v_fmaak_f32 v49, v18, v48, 0x4b400000
	v_fmaak_f32 v50, v19, v48, 0x4b400000
	v_fmaak_f32 v51, v20, v48, 0x4b400000
	v_fmaak_f32 v52, v21, v48, 0x4b400000
	v_perm_b32 v49, v50, v49, s33
	v_perm_b32 v51, v52, v51, s34
	v_or_b32_e32 v49, v49, v51
	global_store_dword v39, v49, s[20:21]
	v_fmaak_f32 v53, v22, v48, 0x4b400000
	v_fmaak_f32 v54, v23, v48, 0x4b400000
	v_fmaak_f32 v55, v24, v48, 0x4b400000
	v_fmaak_f32 v46, v25, v48, 0x4b400000
	v_perm_b32 v53, v54, v53, s33
	v_perm_b32 v55, v46, v55, s34
	v_or_b32_e32 v53, v53, v55
	global_store_dword v39, v53, s[22:23]
	v_fmaak_f32 v49, v26, v48, 0x4b400000
	v_fmaak_f32 v50, v27, v48, 0x4b400000
	v_fmaak_f32 v51, v28, v48, 0x4b400000
	v_fmaak_f32 v52, v29, v48, 0x4b400000
	v_perm_b32 v49, v50, v49, s33
	v_perm_b32 v51, v52, v51, s34
	v_or_b32_e32 v49, v49, v51
	global_store_dword v39, v49, s[24:25]
	v_fmaak_f32 v53, v30, v48, 0x4b400000
	v_fmaak_f32 v54, v31, v48, 0x4b400000
	v_fmaak_f32 v55, v32, v48, 0x4b400000
	v_fmaak_f32 v46, v33, v48, 0x4b400000
	v_perm_b32 v53, v54, v53, s33
	v_perm_b32 v55, v46, v55, s34
	v_or_b32_e32 v53, v53, v55
	global_store_dword v39, v53, s[26:27]
	s_add_u32 s20, s20, 0x400
	s_addc_u32 s21, s21, 0
	s_add_u32 s22, s22, 0x400
	s_addc_u32 s23, s23, 0
	s_add_u32 s24, s24, 0x400
	s_addc_u32 s25, s25, 0
	s_add_u32 s26, s26, 0x400
	s_addc_u32 s27, s27, 0
	s_waitcnt vmcnt(12)
	ds_read_b128 v[18:21], v38 offset:0
	ds_read_b128 v[22:25], v38 offset:1024
	ds_read_b128 v[26:29], v38 offset:2048
	ds_read_b128 v[30:33], v38 offset:3072
	s_waitcnt lgkmcnt(0)
	s_mov_b32 m0, s35
	s_nop 0
	global_load_lds_dwordx4 v34, s[16:17] nt
	global_load_lds_dwordx4 v34, s[16:17] offset:1024 nt
	global_load_lds_dwordx4 v34, s[16:17] offset:2048 nt
	global_load_lds_dwordx4 v35, s[16:17] offset:3072 nt
	s_add_u32 s16, s16, 0x7d00
	s_addc_u32 s17, s17, 0
	v_cndmask_b32_e64 v30, 0, v30, s[18:19]
	v_cndmask_b32_e64 v31, 0, v31, s[18:19]
	v_cndmask_b32_e64 v32, 0, v32, s[18:19]
	v_cndmask_b32_e64 v33, 0, v33, s[18:19]
	v_max3_f32 v41, |v18|, |v19|, |v20|
	v_max3_f32 v42, |v21|, |v22|, |v23|
	v_max3_f32 v43, |v24|, |v25|, |v26|
	v_max3_f32 v44, |v27|, |v28|, |v29|
	v_max3_f32 v45, |v30|, |v31|, |v32|
	v_max3_f32 v41, v41, v42, |v33|
	v_max3_f32 v43, v43, v44, v45
	v_max_f32_e32 v41, v41, v43
	v_pk_add_f32 v[2:3], v[2:3], v[18:19]
	v_pk_add_f32 v[4:5], v[4:5], v[20:21]
	v_max_f32_dpp v41, v41, v41 quad_perm:[1,0,3,2] row_mask:0xf bank_mask:0xf
	v_pk_add_f32 v[6:7], v[6:7], v[22:23]
	v_pk_add_f32 v[8:9], v[8:9], v[24:25]
	v_max_f32_dpp v41, v41, v41 quad_perm:[2,3,0,1] row_mask:0xf bank_mask:0xf
	v_pk_add_f32 v[10:11], v[10:11], v[26:27]
	v_pk_add_f32 v[12:13], v[12:13], v[28:29]
	v_max_f32_dpp v41, v41, v41 row_half_mirror row_mask:0xf bank_mask:0xf
	v_pk_add_f32 v[14:15], v[14:15], v[30:31]
	v_pk_add_f32 v[16:17], v[16:17], v[32:33]
	v_max_f32_dpp v41, v41, v41 row_mirror row_mask:0xf bank_mask:0xf
	s_nop 1
	v_max_f32_dpp v41, v41, v41 row_bcast:15 row_mask:0xa bank_mask:0xf
	s_nop 1
	v_max_f32_dpp v41, v41, v41 row_bcast:31 row_mask:0xc bank_mask:0xf
	s_nop 1
	v_readlane_b32 s28, v41, 63
	s_nop 1
	v_div_scale_f32 v48, s[30:31], s28, s28, v47
	v_rcp_f32_e32 v49, v48
	s_nop 0
	v_fma_f32 v50, -v48, v49, 1.0
	v_fmac_f32_e32 v49, v50, v49
	v_mov_b32_e32 v50, s28
	v_div_scale_f32 v50, vcc, s32, v50, s32
	v_mul_f32_e32 v51, v50, v49
	v_fma_f32 v52, -v48, v51, v50
	v_fmac_f32_e32 v51, v52, v49
	v_fma_f32 v48, -v48, v51, v50
	v_div_fmas_f32 v48, v48, v49, v51
	v_div_fixup_f32 v48, v48, s28, v47
	v_cmp_gt_f32_e64 vcc, s28, 0
	v_writelane_b32 v40, s28, 18
	s_nop 0
	v_cndmask_b32_e32 v48, 0, v48, vcc
	v_fmaak_f32 v49, v18, v48, 0x4b400000
	v_fmaak_f32 v50, v19, v48, 0x4b400000
	v_fmaak_f32 v51, v20, v48, 0x4b400000
	v_fmaak_f32 v52, v21, v48, 0x4b400000
	v_perm_b32 v49, v50, v49, s33
	v_perm_b32 v51, v52, v51, s34
	v_or_b32_e32 v49, v49, v51
	global_store_dword v39, v49, s[20:21]
	v_fmaak_f32 v53, v22, v48, 0x4b400000
	v_fmaak_f32 v54, v23, v48, 0x4b400000
	v_fmaak_f32 v55, v24, v48, 0x4b400000
	v_fmaak_f32 v46, v25, v48, 0x4b400000
	v_perm_b32 v53, v54, v53, s33
	v_perm_b32 v55, v46, v55, s34
	v_or_b32_e32 v53, v53, v55
	global_store_dword v39, v53, s[22:23]
	v_fmaak_f32 v49, v26, v48, 0x4b400000
	v_fmaak_f32 v50, v27, v48, 0x4b400000
	v_fmaak_f32 v51, v28, v48, 0x4b400000
	v_fmaak_f32 v52, v29, v48, 0x4b400000
	v_perm_b32 v49, v50, v49, s33
	v_perm_b32 v51, v52, v51, s34
	v_or_b32_e32 v49, v49, v51
	global_store_dword v39, v49, s[24:25]
	v_fmaak_f32 v53, v30, v48, 0x4b400000
	v_fmaak_f32 v54, v31, v48, 0x4b400000
	v_fmaak_f32 v55, v32, v48, 0x4b400000
	v_fmaak_f32 v46, v33, v48, 0x4b400000
	v_perm_b32 v53, v54, v53, s33
	v_perm_b32 v55, v46, v55, s34
	v_or_b32_e32 v53, v53, v55
	global_store_dword v39, v53, s[26:27]
	s_add_u32 s20, s20, 0x400
	s_addc_u32 s21, s21, 0
	s_add_u32 s22, s22, 0x400
	s_addc_u32 s23, s23, 0
	s_add_u32 s24, s24, 0x400
	s_addc_u32 s25, s25, 0
	s_add_u32 s26, s26, 0x400
	s_addc_u32 s27, s27, 0
	s_waitcnt vmcnt(12)
	ds_read_b128 v[18:21], v38 offset:4096
	ds_read_b128 v[22:25], v38 offset:5120
	ds_read_b128 v[26:29], v38 offset:6144
	ds_read_b128 v[30:33], v38 offset:7168
	s_waitcnt lgkmcnt(0)
	s_mov_b32 m0, s36
	s_nop 0
	global_load_lds_dwordx4 v34, s[16:17] nt
	global_load_lds_dwordx4 v34, s[16:17] offset:1024 nt
	global_load_lds_dwordx4 v34, s[16:17] offset:2048 nt
	global_load_lds_dwordx4 v35, s[16:17] offset:3072 nt
	s_add_u32 s16, s16, 0x7d00
	s_addc_u32 s17, s17, 0
	v_cndmask_b32_e64 v30, 0, v30, s[18:19]
	v_cndmask_b32_e64 v31, 0, v31, s[18:19]
	v_cndmask_b32_e64 v32, 0, v32, s[18:19]
	v_cndmask_b32_e64 v33, 0, v33, s[18:19]
	v_max3_f32 v41, |v18|, |v19|, |v20|
	v_max3_f32 v42, |v21|, |v22|, |v23|
	v_max3_f32 v43, |v24|, |v25|, |v26|
	v_max3_f32 v44, |v27|, |v28|, |v29|
	v_max3_f32 v45, |v30|, |v31|, |v32|
	v_max3_f32 v41, v41, v42, |v33|
	v_max3_f32 v43, v43, v44, v45
	v_max_f32_e32 v41, v41, v43
	v_pk_add_f32 v[2:3], v[2:3], v[18:19]
	v_pk_add_f32 v[4:5], v[4:5], v[20:21]
	v_max_f32_dpp v41, v41, v41 quad_perm:[1,0,3,2] row_mask:0xf bank_mask:0xf
	v_pk_add_f32 v[6:7], v[6:7], v[22:23]
	v_pk_add_f32 v[8:9], v[8:9], v[24:25]
	v_max_f32_dpp v41, v41, v41 quad_perm:[2,3,0,1] row_mask:0xf bank_mask:0xf
	v_pk_add_f32 v[10:11], v[10:11], v[26:27]
	v_pk_add_f32 v[12:13], v[12:13], v[28:29]
	v_max_f32_dpp v41, v41, v41 row_half_mirror row_mask:0xf bank_mask:0xf
	v_pk_add_f32 v[14:15], v[14:15], v[30:31]
	v_pk_add_f32 v[16:17], v[16:17], v[32:33]
	v_max_f32_dpp v41, v41, v41 row_mirror row_mask:0xf bank_mask:0xf
	s_nop 1
	v_max_f32_dpp v41, v41, v41 row_bcast:15 row_mask:0xa bank_mask:0xf
	s_nop 1
	v_max_f32_dpp v41, v41, v41 row_bcast:31 row_mask:0xc bank_mask:0xf
	s_nop 1
	v_readlane_b32 s28, v41, 63
	s_nop 1
	v_div_scale_f32 v48, s[30:31], s28, s28, v47
	v_rcp_f32_e32 v49, v48
	s_nop 0
	v_fma_f32 v50, -v48, v49, 1.0
	v_fmac_f32_e32 v49, v50, v49
	v_mov_b32_e32 v50, s28
	v_div_scale_f32 v50, vcc, s32, v50, s32
	v_mul_f32_e32 v51, v50, v49
	v_fma_f32 v52, -v48, v51, v50
	v_fmac_f32_e32 v51, v52, v49
	v_fma_f32 v48, -v48, v51, v50
	v_div_fmas_f32 v48, v48, v49, v51
	v_div_fixup_f32 v48, v48, s28, v47
	v_cmp_gt_f32_e64 vcc, s28, 0
	v_writelane_b32 v40, s28, 19
	s_nop 0
	v_cndmask_b32_e32 v48, 0, v48, vcc
	v_fmaak_f32 v49, v18, v48, 0x4b400000
	v_fmaak_f32 v50, v19, v48, 0x4b400000
	v_fmaak_f32 v51, v20, v48, 0x4b400000
	v_fmaak_f32 v52, v21, v48, 0x4b400000
	v_perm_b32 v49, v50, v49, s33
	v_perm_b32 v51, v52, v51, s34
	v_or_b32_e32 v49, v49, v51
	global_store_dword v39, v49, s[20:21]
	v_fmaak_f32 v53, v22, v48, 0x4b400000
	v_fmaak_f32 v54, v23, v48, 0x4b400000
	v_fmaak_f32 v55, v24, v48, 0x4b400000
	v_fmaak_f32 v46, v25, v48, 0x4b400000
	v_perm_b32 v53, v54, v53, s33
	v_perm_b32 v55, v46, v55, s34
	v_or_b32_e32 v53, v53, v55
	global_store_dword v39, v53, s[22:23]
	v_fmaak_f32 v49, v26, v48, 0x4b400000
	v_fmaak_f32 v50, v27, v48, 0x4b400000
	v_fmaak_f32 v51, v28, v48, 0x4b400000
	v_fmaak_f32 v52, v29, v48, 0x4b400000
	v_perm_b32 v49, v50, v49, s33
	v_perm_b32 v51, v52, v51, s34
	v_or_b32_e32 v49, v49, v51
	global_store_dword v39, v49, s[24:25]
	v_fmaak_f32 v53, v30, v48, 0x4b400000
	v_fmaak_f32 v54, v31, v48, 0x4b400000
	v_fmaak_f32 v55, v32, v48, 0x4b400000
	v_fmaak_f32 v46, v33, v48, 0x4b400000
	v_perm_b32 v53, v54, v53, s33
	v_perm_b32 v55, v46, v55, s34
	v_or_b32_e32 v53, v53, v55
	global_store_dword v39, v53, s[26:27]
	s_add_u32 s20, s20, 0x400
	s_addc_u32 s21, s21, 0
	s_add_u32 s22, s22, 0x400
	s_addc_u32 s23, s23, 0
	s_add_u32 s24, s24, 0x400
	s_addc_u32 s25, s25, 0
	s_add_u32 s26, s26, 0x400
	s_addc_u32 s27, s27, 0
	s_waitcnt vmcnt(12)
	ds_read_b128 v[18:21], v38 offset:0
	ds_read_b128 v[22:25], v38 offset:1024
	ds_read_b128 v[26:29], v38 offset:2048
	ds_read_b128 v[30:33], v38 offset:3072
	s_waitcnt lgkmcnt(0)
	s_mov_b32 m0, s35
	s_nop 0
	global_load_lds_dwordx4 v34, s[16:17] nt
	global_load_lds_dwordx4 v34, s[16:17] offset:1024 nt
	global_load_lds_dwordx4 v34, s[16:17] offset:2048 nt
	global_load_lds_dwordx4 v35, s[16:17] offset:3072 nt
	s_add_u32 s16, s16, 0x7d00
	s_addc_u32 s17, s17, 0
	v_cndmask_b32_e64 v30, 0, v30, s[18:19]
	v_cndmask_b32_e64 v31, 0, v31, s[18:19]
	v_cndmask_b32_e64 v32, 0, v32, s[18:19]
	v_cndmask_b32_e64 v33, 0, v33, s[18:19]
	v_max3_f32 v41, |v18|, |v19|, |v20|
	v_max3_f32 v42, |v21|, |v22|, |v23|
	v_max3_f32 v43, |v24|, |v25|, |v26|
	v_max3_f32 v44, |v27|, |v28|, |v29|
	v_max3_f32 v45, |v30|, |v31|, |v32|
	v_max3_f32 v41, v41, v42, |v33|
	v_max3_f32 v43, v43, v44, v45
	v_max_f32_e32 v41, v41, v43
	v_pk_add_f32 v[2:3], v[2:3], v[18:19]
	v_pk_add_f32 v[4:5], v[4:5], v[20:21]
	v_max_f32_dpp v41, v41, v41 quad_perm:[1,0,3,2] row_mask:0xf bank_mask:0xf
	v_pk_add_f32 v[6:7], v[6:7], v[22:23]
	v_pk_add_f32 v[8:9], v[8:9], v[24:25]
	v_max_f32_dpp v41, v41, v41 quad_perm:[2,3,0,1] row_mask:0xf bank_mask:0xf
	v_pk_add_f32 v[10:11], v[10:11], v[26:27]
	v_pk_add_f32 v[12:13], v[12:13], v[28:29]
	v_max_f32_dpp v41, v41, v41 row_half_mirror row_mask:0xf bank_mask:0xf
	v_pk_add_f32 v[14:15], v[14:15], v[30:31]
	v_pk_add_f32 v[16:17], v[16:17], v[32:33]
	v_max_f32_dpp v41, v41, v41 row_mirror row_mask:0xf bank_mask:0xf
	s_nop 1
	v_max_f32_dpp v41, v41, v41 row_bcast:15 row_mask:0xa bank_mask:0xf
	s_nop 1
	v_max_f32_dpp v41, v41, v41 row_bcast:31 row_mask:0xc bank_mask:0xf
	s_nop 1
	v_readlane_b32 s28, v41, 63
	s_nop 1
	v_div_scale_f32 v48, s[30:31], s28, s28, v47
	v_rcp_f32_e32 v49, v48
	s_nop 0
	v_fma_f32 v50, -v48, v49, 1.0
	v_fmac_f32_e32 v49, v50, v49
	v_mov_b32_e32 v50, s28
	v_div_scale_f32 v50, vcc, s32, v50, s32
	v_mul_f32_e32 v51, v50, v49
	v_fma_f32 v52, -v48, v51, v50
	v_fmac_f32_e32 v51, v52, v49
	v_fma_f32 v48, -v48, v51, v50
	v_div_fmas_f32 v48, v48, v49, v51
	v_div_fixup_f32 v48, v48, s28, v47
	v_cmp_gt_f32_e64 vcc, s28, 0
	v_writelane_b32 v40, s28, 20
	s_nop 0
	v_cndmask_b32_e32 v48, 0, v48, vcc
	v_fmaak_f32 v49, v18, v48, 0x4b400000
	v_fmaak_f32 v50, v19, v48, 0x4b400000
	v_fmaak_f32 v51, v20, v48, 0x4b400000
	v_fmaak_f32 v52, v21, v48, 0x4b400000
	v_perm_b32 v49, v50, v49, s33
	v_perm_b32 v51, v52, v51, s34
	v_or_b32_e32 v49, v49, v51
	global_store_dword v39, v49, s[20:21]
	v_fmaak_f32 v53, v22, v48, 0x4b400000
	v_fmaak_f32 v54, v23, v48, 0x4b400000
	v_fmaak_f32 v55, v24, v48, 0x4b400000
	v_fmaak_f32 v46, v25, v48, 0x4b400000
	v_perm_b32 v53, v54, v53, s33
	v_perm_b32 v55, v46, v55, s34
	v_or_b32_e32 v53, v53, v55
	global_store_dword v39, v53, s[22:23]
	v_fmaak_f32 v49, v26, v48, 0x4b400000
	v_fmaak_f32 v50, v27, v48, 0x4b400000
	v_fmaak_f32 v51, v28, v48, 0x4b400000
	v_fmaak_f32 v52, v29, v48, 0x4b400000
	v_perm_b32 v49, v50, v49, s33
	v_perm_b32 v51, v52, v51, s34
	v_or_b32_e32 v49, v49, v51
	global_store_dword v39, v49, s[24:25]
	v_fmaak_f32 v53, v30, v48, 0x4b400000
	v_fmaak_f32 v54, v31, v48, 0x4b400000
	v_fmaak_f32 v55, v32, v48, 0x4b400000
	v_fmaak_f32 v46, v33, v48, 0x4b400000
	v_perm_b32 v53, v54, v53, s33
	v_perm_b32 v55, v46, v55, s34
	v_or_b32_e32 v53, v53, v55
	global_store_dword v39, v53, s[26:27]
	s_add_u32 s20, s20, 0x400
	s_addc_u32 s21, s21, 0
	s_add_u32 s22, s22, 0x400
	s_addc_u32 s23, s23, 0
	s_add_u32 s24, s24, 0x400
	s_addc_u32 s25, s25, 0
	s_add_u32 s26, s26, 0x400
	s_addc_u32 s27, s27, 0
	s_waitcnt vmcnt(12)
	ds_read_b128 v[18:21], v38 offset:4096
	ds_read_b128 v[22:25], v38 offset:5120
	ds_read_b128 v[26:29], v38 offset:6144
	ds_read_b128 v[30:33], v38 offset:7168
	s_waitcnt lgkmcnt(0)
	s_mov_b32 m0, s36
	s_nop 0
	global_load_lds_dwordx4 v34, s[16:17] nt
	global_load_lds_dwordx4 v34, s[16:17] offset:1024 nt
	global_load_lds_dwordx4 v34, s[16:17] offset:2048 nt
	global_load_lds_dwordx4 v35, s[16:17] offset:3072 nt
	s_add_u32 s16, s16, 0x7d00
	s_addc_u32 s17, s17, 0
	v_cndmask_b32_e64 v30, 0, v30, s[18:19]
	v_cndmask_b32_e64 v31, 0, v31, s[18:19]
	v_cndmask_b32_e64 v32, 0, v32, s[18:19]
	v_cndmask_b32_e64 v33, 0, v33, s[18:19]
	v_max3_f32 v41, |v18|, |v19|, |v20|
	v_max3_f32 v42, |v21|, |v22|, |v23|
	v_max3_f32 v43, |v24|, |v25|, |v26|
	v_max3_f32 v44, |v27|, |v28|, |v29|
	v_max3_f32 v45, |v30|, |v31|, |v32|
	v_max3_f32 v41, v41, v42, |v33|
	v_max3_f32 v43, v43, v44, v45
	v_max_f32_e32 v41, v41, v43
	v_pk_add_f32 v[2:3], v[2:3], v[18:19]
	v_pk_add_f32 v[4:5], v[4:5], v[20:21]
	v_max_f32_dpp v41, v41, v41 quad_perm:[1,0,3,2] row_mask:0xf bank_mask:0xf
	v_pk_add_f32 v[6:7], v[6:7], v[22:23]
	v_pk_add_f32 v[8:9], v[8:9], v[24:25]
	v_max_f32_dpp v41, v41, v41 quad_perm:[2,3,0,1] row_mask:0xf bank_mask:0xf
	v_pk_add_f32 v[10:11], v[10:11], v[26:27]
	v_pk_add_f32 v[12:13], v[12:13], v[28:29]
	v_max_f32_dpp v41, v41, v41 row_half_mirror row_mask:0xf bank_mask:0xf
	v_pk_add_f32 v[14:15], v[14:15], v[30:31]
	v_pk_add_f32 v[16:17], v[16:17], v[32:33]
	v_max_f32_dpp v41, v41, v41 row_mirror row_mask:0xf bank_mask:0xf
	s_nop 1
	v_max_f32_dpp v41, v41, v41 row_bcast:15 row_mask:0xa bank_mask:0xf
	s_nop 1
	v_max_f32_dpp v41, v41, v41 row_bcast:31 row_mask:0xc bank_mask:0xf
	s_nop 1
	v_readlane_b32 s28, v41, 63
	s_nop 1
	v_div_scale_f32 v48, s[30:31], s28, s28, v47
	v_rcp_f32_e32 v49, v48
	s_nop 0
	v_fma_f32 v50, -v48, v49, 1.0
	v_fmac_f32_e32 v49, v50, v49
	v_mov_b32_e32 v50, s28
	v_div_scale_f32 v50, vcc, s32, v50, s32
	v_mul_f32_e32 v51, v50, v49
	v_fma_f32 v52, -v48, v51, v50
	v_fmac_f32_e32 v51, v52, v49
	v_fma_f32 v48, -v48, v51, v50
	v_div_fmas_f32 v48, v48, v49, v51
	v_div_fixup_f32 v48, v48, s28, v47
	v_cmp_gt_f32_e64 vcc, s28, 0
	v_writelane_b32 v40, s28, 21
	s_nop 0
	v_cndmask_b32_e32 v48, 0, v48, vcc
	v_fmaak_f32 v49, v18, v48, 0x4b400000
	v_fmaak_f32 v50, v19, v48, 0x4b400000
	v_fmaak_f32 v51, v20, v48, 0x4b400000
	v_fmaak_f32 v52, v21, v48, 0x4b400000
	v_perm_b32 v49, v50, v49, s33
	v_perm_b32 v51, v52, v51, s34
	v_or_b32_e32 v49, v49, v51
	global_store_dword v39, v49, s[20:21]
	v_fmaak_f32 v53, v22, v48, 0x4b400000
	v_fmaak_f32 v54, v23, v48, 0x4b400000
	v_fmaak_f32 v55, v24, v48, 0x4b400000
	v_fmaak_f32 v46, v25, v48, 0x4b400000
	v_perm_b32 v53, v54, v53, s33
	v_perm_b32 v55, v46, v55, s34
	v_or_b32_e32 v53, v53, v55
	global_store_dword v39, v53, s[22:23]
	v_fmaak_f32 v49, v26, v48, 0x4b400000
	v_fmaak_f32 v50, v27, v48, 0x4b400000
	v_fmaak_f32 v51, v28, v48, 0x4b400000
	v_fmaak_f32 v52, v29, v48, 0x4b400000
	v_perm_b32 v49, v50, v49, s33
	v_perm_b32 v51, v52, v51, s34
	v_or_b32_e32 v49, v49, v51
	global_store_dword v39, v49, s[24:25]
	v_fmaak_f32 v53, v30, v48, 0x4b400000
	v_fmaak_f32 v54, v31, v48, 0x4b400000
	v_fmaak_f32 v55, v32, v48, 0x4b400000
	v_fmaak_f32 v46, v33, v48, 0x4b400000
	v_perm_b32 v53, v54, v53, s33
	v_perm_b32 v55, v46, v55, s34
	v_or_b32_e32 v53, v53, v55
	global_store_dword v39, v53, s[26:27]
	s_add_u32 s20, s20, 0x400
	s_addc_u32 s21, s21, 0
	s_add_u32 s22, s22, 0x400
	s_addc_u32 s23, s23, 0
	s_add_u32 s24, s24, 0x400
	s_addc_u32 s25, s25, 0
	s_add_u32 s26, s26, 0x400
	s_addc_u32 s27, s27, 0
	s_waitcnt vmcnt(12)
	ds_read_b128 v[18:21], v38 offset:0
	ds_read_b128 v[22:25], v38 offset:1024
	ds_read_b128 v[26:29], v38 offset:2048
	ds_read_b128 v[30:33], v38 offset:3072
	s_waitcnt lgkmcnt(0)
	s_cmp_eq_u32 s29, 1
	s_cbranch_scc0 .Lk1_nodma24
	s_mov_b32 m0, s35
	s_nop 0
	global_load_lds_dwordx4 v34, s[16:17] nt
	global_load_lds_dwordx4 v34, s[16:17] offset:1024 nt
	global_load_lds_dwordx4 v34, s[16:17] offset:2048 nt
	global_load_lds_dwordx4 v35, s[16:17] offset:3072 nt
	s_add_u32 s16, s16, 0x7d00
	s_addc_u32 s17, s17, 0
.Lk1_nodma24:
	v_cndmask_b32_e64 v30, 0, v30, s[18:19]
	v_cndmask_b32_e64 v31, 0, v31, s[18:19]
	v_cndmask_b32_e64 v32, 0, v32, s[18:19]
	v_cndmask_b32_e64 v33, 0, v33, s[18:19]
	v_max3_f32 v41, |v18|, |v19|, |v20|
	v_max3_f32 v42, |v21|, |v22|, |v23|
	v_max3_f32 v43, |v24|, |v25|, |v26|
	v_max3_f32 v44, |v27|, |v28|, |v29|
	v_max3_f32 v45, |v30|, |v31|, |v32|
	v_max3_f32 v41, v41, v42, |v33|
	v_max3_f32 v43, v43, v44, v45
	v_max_f32_e32 v41, v41, v43
	v_pk_add_f32 v[2:3], v[2:3], v[18:19]
	v_pk_add_f32 v[4:5], v[4:5], v[20:21]
	v_max_f32_dpp v41, v41, v41 quad_perm:[1,0,3,2] row_mask:0xf bank_mask:0xf
	v_pk_add_f32 v[6:7], v[6:7], v[22:23]
	v_pk_add_f32 v[8:9], v[8:9], v[24:25]
	v_max_f32_dpp v41, v41, v41 quad_perm:[2,3,0,1] row_mask:0xf bank_mask:0xf
	v_pk_add_f32 v[10:11], v[10:11], v[26:27]
	v_pk_add_f32 v[12:13], v[12:13], v[28:29]
	v_max_f32_dpp v41, v41, v41 row_half_mirror row_mask:0xf bank_mask:0xf
	v_pk_add_f32 v[14:15], v[14:15], v[30:31]
	v_pk_add_f32 v[16:17], v[16:17], v[32:33]
	v_max_f32_dpp v41, v41, v41 row_mirror row_mask:0xf bank_mask:0xf
	s_nop 1
	v_max_f32_dpp v41, v41, v41 row_bcast:15 row_mask:0xa bank_mask:0xf
	s_nop 1
	v_max_f32_dpp v41, v41, v41 row_bcast:31 row_mask:0xc bank_mask:0xf
	s_nop 1
	v_readlane_b32 s28, v41, 63
	s_nop 1
	v_div_scale_f32 v48, s[30:31], s28, s28, v47
	v_rcp_f32_e32 v49, v48
	s_nop 0
	v_fma_f32 v50, -v48, v49, 1.0
	v_fmac_f32_e32 v49, v50, v49
	v_mov_b32_e32 v50, s28
	v_div_scale_f32 v50, vcc, s32, v50, s32
	v_mul_f32_e32 v51, v50, v49
	v_fma_f32 v52, -v48, v51, v50
	v_fmac_f32_e32 v51, v52, v49
	v_fma_f32 v48, -v48, v51, v50
	v_div_fmas_f32 v48, v48, v49, v51
	v_div_fixup_f32 v48, v48, s28, v47
	v_cmp_gt_f32_e64 vcc, s28, 0
	v_writelane_b32 v40, s28, 22
	s_nop 0
	v_cndmask_b32_e32 v48, 0, v48, vcc
	v_fmaak_f32 v49, v18, v48, 0x4b400000
	v_fmaak_f32 v50, v19, v48, 0x4b400000
	v_fmaak_f32 v51, v20, v48, 0x4b400000
	v_fmaak_f32 v52, v21, v48, 0x4b400000
	v_perm_b32 v49, v50, v49, s33
	v_perm_b32 v51, v52, v51, s34
	v_or_b32_e32 v49, v49, v51
	global_store_dword v39, v49, s[20:21]
	v_fmaak_f32 v53, v22, v48, 0x4b400000
	v_fmaak_f32 v54, v23, v48, 0x4b400000
	v_fmaak_f32 v55, v24, v48, 0x4b400000
	v_fmaak_f32 v46, v25, v48, 0x4b400000
	v_perm_b32 v53, v54, v53, s33
	v_perm_b32 v55, v46, v55, s34
	v_or_b32_e32 v53, v53, v55
	global_store_dword v39, v53, s[22:23]
	v_fmaak_f32 v49, v26, v48, 0x4b400000
	v_fmaak_f32 v50, v27, v48, 0x4b400000
	v_fmaak_f32 v51, v28, v48, 0x4b400000
	v_fmaak_f32 v52, v29, v48, 0x4b400000
	v_perm_b32 v49, v50, v49, s33
	v_perm_b32 v51, v52, v51, s34
	v_or_b32_e32 v49, v49, v51
	global_store_dword v39, v49, s[24:25]
	v_fmaak_f32 v53, v30, v48, 0x4b400000
	v_fmaak_f32 v54, v31, v48, 0x4b400000
	v_fmaak_f32 v55, v32, v48, 0x4b400000
	v_fmaak_f32 v46, v33, v48, 0x4b400000
	v_perm_b32 v53, v54, v53, s33
	v_perm_b32 v55, v46, v55, s34
	v_or_b32_e32 v53, v53, v55
	global_store_dword v39, v53, s[26:27]
	s_add_u32 s20, s20, 0x400
	s_addc_u32 s21, s21, 0
	s_add_u32 s22, s22, 0x400
	s_addc_u32 s23, s23, 0
	s_add_u32 s24, s24, 0x400
	s_addc_u32 s25, s25, 0
	s_add_u32 s26, s26, 0x400
	s_addc_u32 s27, s27, 0
	s_waitcnt vmcnt(8)
	ds_read_b128 v[18:21], v38 offset:4096
	ds_read_b128 v[22:25], v38 offset:5120
	ds_read_b128 v[26:29], v38 offset:6144
	ds_read_b128 v[30:33], v38 offset:7168
	s_waitcnt lgkmcnt(0)
	v_cndmask_b32_e64 v30, 0, v30, s[18:19]
	v_cndmask_b32_e64 v31, 0, v31, s[18:19]
	v_cndmask_b32_e64 v32, 0, v32, s[18:19]
	v_cndmask_b32_e64 v33, 0, v33, s[18:19]
	v_max3_f32 v41, |v18|, |v19|, |v20|
	v_max3_f32 v42, |v21|, |v22|, |v23|
	v_max3_f32 v43, |v24|, |v25|, |v26|
	v_max3_f32 v44, |v27|, |v28|, |v29|
	v_max3_f32 v45, |v30|, |v31|, |v32|
	v_max3_f32 v41, v41, v42, |v33|
	v_max3_f32 v43, v43, v44, v45
	v_max_f32_e32 v41, v41, v43
	v_pk_add_f32 v[2:3], v[2:3], v[18:19]
	v_pk_add_f32 v[4:5], v[4:5], v[20:21]
	v_max_f32_dpp v41, v41, v41 quad_perm:[1,0,3,2] row_mask:0xf bank_mask:0xf
	v_pk_add_f32 v[6:7], v[6:7], v[22:23]
	v_pk_add_f32 v[8:9], v[8:9], v[24:25]
	v_max_f32_dpp v41, v41, v41 quad_perm:[2,3,0,1] row_mask:0xf bank_mask:0xf
	v_pk_add_f32 v[10:11], v[10:11], v[26:27]
	v_pk_add_f32 v[12:13], v[12:13], v[28:29]
	v_max_f32_dpp v41, v41, v41 row_half_mirror row_mask:0xf bank_mask:0xf
	v_pk_add_f32 v[14:15], v[14:15], v[30:31]
	v_pk_add_f32 v[16:17], v[16:17], v[32:33]
	v_max_f32_dpp v41, v41, v41 row_mirror row_mask:0xf bank_mask:0xf
	s_nop 1
	v_max_f32_dpp v41, v41, v41 row_bcast:15 row_mask:0xa bank_mask:0xf
	s_nop 1
	v_max_f32_dpp v41, v41, v41 row_bcast:31 row_mask:0xc bank_mask:0xf
	s_nop 1
	v_readlane_b32 s28, v41, 63
	s_nop 1
	v_div_scale_f32 v48, s[30:31], s28, s28, v47
	v_rcp_f32_e32 v49, v48
	s_nop 0
	v_fma_f32 v50, -v48, v49, 1.0
	v_fmac_f32_e32 v49, v50, v49
	v_mov_b32_e32 v50, s28
	v_div_scale_f32 v50, vcc, s32, v50, s32
	v_mul_f32_e32 v51, v50, v49
	v_fma_f32 v52, -v48, v51, v50
	v_fmac_f32_e32 v51, v52, v49
	v_fma_f32 v48, -v48, v51, v50
	v_div_fmas_f32 v48, v48, v49, v51
	v_div_fixup_f32 v48, v48, s28, v47
	v_cmp_gt_f32_e64 vcc, s28, 0
	v_writelane_b32 v40, s28, 23
	s_nop 0
	v_cndmask_b32_e32 v48, 0, v48, vcc
	v_fmaak_f32 v49, v18, v48, 0x4b400000
	v_fmaak_f32 v50, v19, v48, 0x4b400000
	v_fmaak_f32 v51, v20, v48, 0x4b400000
	v_fmaak_f32 v52, v21, v48, 0x4b400000
	v_perm_b32 v49, v50, v49, s33
	v_perm_b32 v51, v52, v51, s34
	v_or_b32_e32 v49, v49, v51
	global_store_dword v39, v49, s[20:21]
	v_fmaak_f32 v53, v22, v48, 0x4b400000
	v_fmaak_f32 v54, v23, v48, 0x4b400000
	v_fmaak_f32 v55, v24, v48, 0x4b400000
	v_fmaak_f32 v46, v25, v48, 0x4b400000
	v_perm_b32 v53, v54, v53, s33
	v_perm_b32 v55, v46, v55, s34
	v_or_b32_e32 v53, v53, v55
	global_store_dword v39, v53, s[22:23]
	v_fmaak_f32 v49, v26, v48, 0x4b400000
	v_fmaak_f32 v50, v27, v48, 0x4b400000
	v_fmaak_f32 v51, v28, v48, 0x4b400000
	v_fmaak_f32 v52, v29, v48, 0x4b400000
	v_perm_b32 v49, v50, v49, s33
	v_perm_b32 v51, v52, v51, s34
	v_or_b32_e32 v49, v49, v51
	global_store_dword v39, v49, s[24:25]
	v_fmaak_f32 v53, v30, v48, 0x4b400000
	v_fmaak_f32 v54, v31, v48, 0x4b400000
	v_fmaak_f32 v55, v32, v48, 0x4b400000
	v_fmaak_f32 v46, v33, v48, 0x4b400000
	v_perm_b32 v53, v54, v53, s33
	v_perm_b32 v55, v46, v55, s34
	v_or_b32_e32 v53, v53, v55
	global_store_dword v39, v53, s[26:27]
	s_add_u32 s20, s20, 0x400
	s_addc_u32 s21, s21, 0
	s_add_u32 s22, s22, 0x400
	s_addc_u32 s23, s23, 0
	s_add_u32 s24, s24, 0x400
	s_addc_u32 s25, s25, 0
	s_add_u32 s26, s26, 0x400
	s_addc_u32 s27, s27, 0
	s_cmp_eq_u32 s29, 1
	s_cbranch_scc0 .Lk1_flush
	s_waitcnt vmcnt(8)
	ds_read_b128 v[18:21], v38 offset:0
	ds_read_b128 v[22:25], v38 offset:1024
	ds_read_b128 v[26:29], v38 offset:2048
	ds_read_b128 v[30:33], v38 offset:3072
	s_waitcnt lgkmcnt(0)
	v_cndmask_b32_e64 v30, 0, v30, s[18:19]
	v_cndmask_b32_e64 v31, 0, v31, s[18:19]
	v_cndmask_b32_e64 v32, 0, v32, s[18:19]
	v_cndmask_b32_e64 v33, 0, v33, s[18:19]
	v_max3_f32 v41, |v18|, |v19|, |v20|
	v_max3_f32 v42, |v21|, |v22|, |v23|
	v_max3_f32 v43, |v24|, |v25|, |v26|
	v_max3_f32 v44, |v27|, |v28|, |v29|
	v_max3_f32 v45, |v30|, |v31|, |v32|
	v_max3_f32 v41, v41, v42, |v33|
	v_max3_f32 v43, v43, v44, v45
	v_max_f32_e32 v41, v41, v43
	v_pk_add_f32 v[2:3], v[2:3], v[18:19]
	v_pk_add_f32 v[4:5], v[4:5], v[20:21]
	v_max_f32_dpp v41, v41, v41 quad_perm:[1,0,3,2] row_mask:0xf bank_mask:0xf
	v_pk_add_f32 v[6:7], v[6:7], v[22:23]
	v_pk_add_f32 v[8:9], v[8:9], v[24:25]
	v_max_f32_dpp v41, v41, v41 quad_perm:[2,3,0,1] row_mask:0xf bank_mask:0xf
	v_pk_add_f32 v[10:11], v[10:11], v[26:27]
	v_pk_add_f32 v[12:13], v[12:13], v[28:29]
	v_max_f32_dpp v41, v41, v41 row_half_mirror row_mask:0xf bank_mask:0xf
	v_pk_add_f32 v[14:15], v[14:15], v[30:31]
	v_pk_add_f32 v[16:17], v[16:17], v[32:33]
	v_max_f32_dpp v41, v41, v41 row_mirror row_mask:0xf bank_mask:0xf
	s_nop 1
	v_max_f32_dpp v41, v41, v41 row_bcast:15 row_mask:0xa bank_mask:0xf
	s_nop 1
	v_max_f32_dpp v41, v41, v41 row_bcast:31 row_mask:0xc bank_mask:0xf
	s_nop 1
	v_readlane_b32 s28, v41, 63
	s_nop 1
	v_div_scale_f32 v48, s[30:31], s28, s28, v47
	v_rcp_f32_e32 v49, v48
	s_nop 0
	v_fma_f32 v50, -v48, v49, 1.0
	v_fmac_f32_e32 v49, v50, v49
	v_mov_b32_e32 v50, s28
	v_div_scale_f32 v50, vcc, s32, v50, s32
	v_mul_f32_e32 v51, v50, v49
	v_fma_f32 v52, -v48, v51, v50
	v_fmac_f32_e32 v51, v52, v49
	v_fma_f32 v48, -v48, v51, v50
	v_div_fmas_f32 v48, v48, v49, v51
	v_div_fixup_f32 v48, v48, s28, v47
	v_cmp_gt_f32_e64 vcc, s28, 0
	v_writelane_b32 v40, s28, 24
	s_nop 0
	v_cndmask_b32_e32 v48, 0, v48, vcc
	v_fmaak_f32 v49, v18, v48, 0x4b400000
	v_fmaak_f32 v50, v19, v48, 0x4b400000
	v_fmaak_f32 v51, v20, v48, 0x4b400000
	v_fmaak_f32 v52, v21, v48, 0x4b400000
	v_perm_b32 v49, v50, v49, s33
	v_perm_b32 v51, v52, v51, s34
	v_or_b32_e32 v49, v49, v51
	global_store_dword v39, v49, s[20:21]
	v_fmaak_f32 v53, v22, v48, 0x4b400000
	v_fmaak_f32 v54, v23, v48, 0x4b400000
	v_fmaak_f32 v55, v24, v48, 0x4b400000
	v_fmaak_f32 v46, v25, v48, 0x4b400000
	v_perm_b32 v53, v54, v53, s33
	v_perm_b32 v55, v46, v55, s34
	v_or_b32_e32 v53, v53, v55
	global_store_dword v39, v53, s[22:23]
	v_fmaak_f32 v49, v26, v48, 0x4b400000
	v_fmaak_f32 v50, v27, v48, 0x4b400000
	v_fmaak_f32 v51, v28, v48, 0x4b400000
	v_fmaak_f32 v52, v29, v48, 0x4b400000
	v_perm_b32 v49, v50, v49, s33
	v_perm_b32 v51, v52, v51, s34
	v_or_b32_e32 v49, v49, v51
	global_store_dword v39, v49, s[24:25]
	v_fmaak_f32 v53, v30, v48, 0x4b400000
	v_fmaak_f32 v54, v31, v48, 0x4b400000
	v_fmaak_f32 v55, v32, v48, 0x4b400000
	v_fmaak_f32 v46, v33, v48, 0x4b400000
	v_perm_b32 v53, v54, v53, s33
	v_perm_b32 v55, v46, v55, s34
	v_or_b32_e32 v53, v53, v55
	global_store_dword v39, v53, s[26:27]
	s_add_u32 s20, s20, 0x400
	s_addc_u32 s21, s21, 0
	s_add_u32 s22, s22, 0x400
	s_addc_u32 s23, s23, 0
	s_add_u32 s24, s24, 0x400
	s_addc_u32 s25, s25, 0
	s_add_u32 s26, s26, 0x400
	s_addc_u32 s27, s27, 0
.Lk1_flush:
	s_mov_b64 s[20:21], s[40:41]
	s_add_u32 s22, s20, 0x186a000
	s_addc_u32 s23, s21, 0
	s_add_u32 s24, s22, 0x186a000
	s_addc_u32 s25, s23, 0
	s_add_u32 s26, s24, 0x186a000
	s_addc_u32 s27, s25, 0
	global_store_dword v39, v56, s[20:21]
	global_store_dword v39, v57, s[22:23]
	global_store_dword v39, v58, s[24:25]
	global_store_dword v39, v59, s[26:27]
	global_store_dword v39, v60, s[20:21] offset:1024
	global_store_dword v39, v61, s[22:23] offset:1024
	global_store_dword v39, v62, s[24:25] offset:1024
	global_store_dword v39, v63, s[26:27] offset:1024
	global_store_dword v39, v64, s[20:21] offset:2048
	global_store_dword v39, v65, s[22:23] offset:2048
	global_store_dword v39, v66, s[24:25] offset:2048
	global_store_dword v39, v67, s[26:27] offset:2048
	global_store_dword v39, v68, s[20:21] offset:3072
	global_store_dword v39, v69, s[22:23] offset:3072
	global_store_dword v39, v70, s[24:25] offset:3072
	global_store_dword v39, v71, s[26:27] offset:3072
	s_add_u32 s20, s20, 0x1000
	s_addc_u32 s21, s21, 0
	s_add_u32 s22, s22, 0x1000
	s_addc_u32 s23, s23, 0
	s_add_u32 s24, s24, 0x1000
	s_addc_u32 s25, s25, 0
	s_add_u32 s26, s26, 0x1000
	s_addc_u32 s27, s27, 0
	global_store_dword v39, v72, s[20:21]
	global_store_dword v39, v73, s[22:23]
	global_store_dword v39, v74, s[24:25]
	global_store_dword v39, v75, s[26:27]
	global_store_dword v39, v76, s[20:21] offset:1024
	global_store_dword v39, v77, s[22:23] offset:1024
	global_store_dword v39, v78, s[24:25] offset:1024
	global_store_dword v39, v79, s[26:27] offset:1024
	global_store_dword v39, v80, s[20:21] offset:2048
	global_store_dword v39, v81, s[22:23] offset:2048
	global_store_dword v39, v82, s[24:25] offset:2048
	global_store_dword v39, v83, s[26:27] offset:2048
	global_store_dword v39, v84, s[20:21] offset:3072
	global_store_dword v39, v85, s[22:23] offset:3072
	global_store_dword v39, v86, s[24:25] offset:3072
	global_store_dword v39, v87, s[26:27] offset:3072
	s_add_u32 s20, s20, 0x1000
	s_addc_u32 s21, s21, 0
	s_add_u32 s22, s22, 0x1000
	s_addc_u32 s23, s23, 0
	s_add_u32 s24, s24, 0x1000
	s_addc_u32 s25, s25, 0
	s_add_u32 s26, s26, 0x1000
	s_addc_u32 s27, s27, 0
	global_store_dword v39, v88, s[20:21]
	global_store_dword v39, v89, s[22:23]
	global_store_dword v39, v90, s[24:25]
	global_store_dword v39, v91, s[26:27]
	global_store_dword v39, v92, s[20:21] offset:1024
	global_store_dword v39, v93, s[22:23] offset:1024
	global_store_dword v39, v94, s[24:25] offset:1024
	global_store_dword v39, v95, s[26:27] offset:1024
	global_store_dword v39, v96, s[20:21] offset:2048
	global_store_dword v39, v97, s[22:23] offset:2048
	global_store_dword v39, v98, s[24:25] offset:2048
	global_store_dword v39, v99, s[26:27] offset:2048
	global_store_dword v39, v100, s[20:21] offset:3072
	global_store_dword v39, v101, s[22:23] offset:3072
	global_store_dword v39, v102, s[24:25] offset:3072
	global_store_dword v39, v103, s[26:27] offset:3072
	s_add_u32 s20, s20, 0x1000
	s_addc_u32 s21, s21, 0
	s_add_u32 s22, s22, 0x1000
	s_addc_u32 s23, s23, 0
	s_add_u32 s24, s24, 0x1000
	s_addc_u32 s25, s25, 0
	s_add_u32 s26, s26, 0x1000
	s_addc_u32 s27, s27, 0
	global_store_dword v39, v104, s[20:21]
	global_store_dword v39, v105, s[22:23]
	global_store_dword v39, v106, s[24:25]
	global_store_dword v39, v107, s[26:27]
	global_store_dword v39, v108, s[20:21] offset:1024
	global_store_dword v39, v109, s[22:23] offset:1024
	global_store_dword v39, v110, s[24:25] offset:1024
	global_store_dword v39, v111, s[26:27] offset:1024
	global_store_dword v39, v112, s[20:21] offset:2048
	global_store_dword v39, v113, s[22:23] offset:2048
	global_store_dword v39, v114, s[24:25] offset:2048
	global_store_dword v39, v115, s[26:27] offset:2048
	v_mul_f32_e32 v40, 0x3c010204, v40
	v_lshlrev_b32_e32 v41, 5, v1
	s_add_u32 s15, s12, s14
	s_lshl_b32 s15, s15, 2
	s_add_u32 s8, s8, s15
	s_addc_u32 s9, s9, 0
	s_add_u32 s15, s29, 24
	v_cmp_gt_u32_e32 vcc, s15, v1
	s_and_saveexec_b64 s[38:39], vcc
	global_store_dword v41, v40, s[8:9]
	s_mov_b64 exec, s[38:39]
	s_lshl_b32 s15, s14, 12
	v_add_u32_e32 v41, s15, v34
	s_barrier
	ds_write_b128 v41, v[2:5]
	ds_write_b128 v41, v[6:9] offset:1024
	ds_write_b128 v41, v[10:13] offset:2048
	ds_write_b128 v41, v[14:17] offset:3072
	s_waitcnt lgkmcnt(0)
	s_barrier
	s_movk_i32 s15, 0x100
	v_cmp_gt_u32_e32 vcc, s15, v0
	s_and_saveexec_b64 s[38:39], vcc
	s_cbranch_execz .Lk1_end
	v_lshlrev_b32_e32 v16, 4, v0
	ds_read_b128 v[2:5], v16
	ds_read_b128 v[18:21], v16 offset:4096
	ds_read_b128 v[22:25], v16 offset:8192
	ds_read_b128 v[26:29], v16 offset:12288
	ds_read_b128 v[30:33], v16 offset:16384
	ds_read_b128 v[34:37], v16 offset:20480
	ds_read_b128 v[38:41], v16 offset:24576
	ds_read_b128 v[42:45], v16 offset:28672
	s_waitcnt lgkmcnt(6)
	v_pk_add_f32 v[2:3], v[2:3], v[18:19]
	v_pk_add_f32 v[4:5], v[4:5], v[20:21]
	s_waitcnt lgkmcnt(5)
	v_pk_add_f32 v[2:3], v[2:3], v[22:23]
	v_pk_add_f32 v[4:5], v[4:5], v[24:25]
	s_waitcnt lgkmcnt(4)
	v_pk_add_f32 v[2:3], v[2:3], v[26:27]
	v_pk_add_f32 v[4:5], v[4:5], v[28:29]
	s_waitcnt lgkmcnt(3)
	v_pk_add_f32 v[2:3], v[2:3], v[30:31]
	v_pk_add_f32 v[4:5], v[4:5], v[32:33]
	s_waitcnt lgkmcnt(2)
	v_pk_add_f32 v[2:3], v[2:3], v[34:35]
	v_pk_add_f32 v[4:5], v[4:5], v[36:37]
	s_waitcnt lgkmcnt(1)
	v_pk_add_f32 v[2:3], v[2:3], v[38:39]
	v_pk_add_f32 v[4:5], v[4:5], v[40:41]
	s_waitcnt lgkmcnt(0)
	v_pk_add_f32 v[2:3], v[2:3], v[42:43]
	v_pk_add_f32 v[4:5], v[4:5], v[44:45]
	s_lshl_b32 s15, s2, 12
	s_add_u32 s10, s10, s15
	s_addc_u32 s11, s11, 0
	global_store_dwordx4 v16, v[2:5], s[10:11]

	.amdhsa_kernel _Z12k1_colsum_q8PKfPjPfS2_
		.amdhsa_group_segment_fixed_size 65536
		.amdhsa_private_segment_fixed_size 0
		.amdhsa_kernarg_size 32
		.amdhsa_user_sgpr_count 2
		.amdhsa_user_sgpr_dispatch_ptr 0
		.amdhsa_user_sgpr_queue_ptr 0
		.amdhsa_user_sgpr_kernarg_segment_ptr 1
		.amdhsa_user_sgpr_dispatch_id 0
		.amdhsa_user_sgpr_kernarg_preload_length 0
		.amdhsa_user_sgpr_kernarg_preload_offset 0
		.amdhsa_user_sgpr_private_segment_size 0
		.amdhsa_uses_dynamic_stack 0
		.amdhsa_enable_private_segment 0
		.amdhsa_system_sgpr_workgroup_id_x 1
		.amdhsa_system_sgpr_workgroup_id_y 0
		.amdhsa_system_sgpr_workgroup_id_z 0
		.amdhsa_system_sgpr_workgroup_info 0
		.amdhsa_system_vgpr_workitem_id 0
		.amdhsa_next_free_vgpr 128
		.amdhsa_next_free_sgpr 96
		.amdhsa_accum_offset 128
		.amdhsa_reserve_vcc 1
		.amdhsa_float_round_mode_32 0
		.amdhsa_float_round_mode_16_64 0
		.amdhsa_float_denorm_mode_32 3
		.amdhsa_float_denorm_mode_16_64 3
		.amdhsa_dx10_clamp 1
		.amdhsa_ieee_mode 1
		.amdhsa_fp16_overflow 0
		.amdhsa_tg_split 0
		.amdhsa_exception_fp_ieee_invalid_op 0
		.amdhsa_exception_fp_denorm_src 0
		.amdhsa_exception_fp_ieee_div_zero 0
		.amdhsa_exception_fp_ieee_overflow 0
		.amdhsa_exception_fp_ieee_underflow 0
		.amdhsa_exception_fp_ieee_inexact 0
		.amdhsa_exception_int_div_zero 0
	.end_amdhsa_kernel

amdhsa.kernels:
  - .agpr_count:     0
    .args:
      - .address_space:  global
        .offset:         0
        .size:           8
        .value_kind:     global_buffer
      - .actual_access:  write_only
        .address_space:  global
        .offset:         8
        .size:           8
        .value_kind:     global_buffer
      - .actual_access:  write_only
        .address_space:  global
        .offset:         16
        .size:           8
        .value_kind:     global_buffer
      - .actual_access:  write_only
        .address_space:  global
        .offset:         24
        .size:           8
        .value_kind:     global_buffer
    .group_segment_fixed_size: 65536
    .kernarg_segment_align: 8
    .kernarg_segment_size: 32
    .language:       OpenCL C
    .language_version:
      - 2
      - 0
    .max_flat_workgroup_size: 512
    .name:           _Z12k1_colsum_q8PKfPjPfS2_
    .private_segment_fixed_size: 0
    .sgpr_count:     44
    .sgpr_spill_count: 0
    .symbol:         _Z12k1_colsum_q8PKfPjPfS2_.kd
    .uniform_work_group_size: 1
    .uses_dynamic_stack: false
    .vgpr_count:     128
    .vgpr_spill_count: 0
    .wavefront_size: 64
  - .agpr_count:     0
    .args:
      - .actual_access:  read_only
        .address_space:  global
        .offset:         0
        .size:           8
        .value_kind:     global_buffer
      - .actual_access:  write_only
        .address_space:  global
        .offset:         8
        .size:           8
        .value_kind:     global_buffer
      - .actual_access:  write_only
        .address_space:  global
        .offset:         16
        .size:           8
        .value_kind:     global_buffer
      - .actual_access:  write_only
        .address_space:  global
        .offset:         24
        .size:           8
        .value_kind:     global_buffer
      - .actual_access:  write_only
        .address_space:  global
        .offset:         32
        .size:           8
        .value_kind:     global_buffer
      - .actual_access:  read_only
        .address_space:  global
        .offset:         40
        .size:           8
        .value_kind:     global_buffer
      - .actual_access:  read_only
        .address_space:  global
        .offset:         48
        .size:           8
        .value_kind:     global_buffer
      - .actual_access:  read_only
        .address_space:  global
        .offset:         56
        .size:           8
        .value_kind:     global_buffer
      - .actual_access:  write_only
        .address_space:  global
        .offset:         64
        .size:           8
        .value_kind:     global_buffer
      - .actual_access:  write_only
        .address_space:  global
        .offset:         72
        .size:           8
        .value_kind:     global_buffer
    .group_segment_fixed_size: 1024
    .kernarg_segment_align: 8
    .kernarg_segment_size: 80
    .language:       OpenCL C
    .language_version:
      - 2
      - 0
    .max_flat_workgroup_size: 256
    .name:           _Z12k2_reduce_csPKfPfS1_PiS1_S0_PKiS4_S1_S1_
    .private_segment_fixed_size: 0
    .sgpr_count:     22
    .sgpr_spill_count: 0
    .symbol:         _Z12k2_reduce_csPKfPfS1_PiS1_S0_PKiS4_S1_S1_.kd
    .uniform_work_group_size: 1
    .uses_dynamic_stack: false
    .vgpr_count:     36
    .vgpr_spill_count: 0
    .wavefront_size: 64
  - .agpr_count:     0
    .args:
      - .actual_access:  read_only
        .address_space:  global
        .offset:         0
        .size:           8
        .value_kind:     global_buffer
      - .actual_access:  read_only
        .address_space:  global
        .offset:         8
        .size:           8
        .value_kind:     global_buffer
      - .actual_access:  read_only
        .address_space:  global
        .offset:         16
        .size:           8
        .value_kind:     global_buffer
      - .actual_access:  read_only
        .address_space:  global
        .offset:         24
        .size:           8
        .value_kind:     global_buffer
      - .address_space:  global
        .offset:         32
        .size:           8
        .value_kind:     global_buffer
      - .address_space:  global
        .offset:         40
        .size:           8
        .value_kind:     global_buffer
    .group_segment_fixed_size: 0
    .kernarg_segment_align: 8
    .kernarg_segment_size: 48
    .language:       OpenCL C
    .language_version:
      - 2
      - 0
    .max_flat_workgroup_size: 256
    .name:           _Z15k3_pairs_slicedPKDv4_jPKfPKiS5_PiPf
    .private_segment_fixed_size: 0
    .sgpr_count:     26
    .sgpr_spill_count: 0
    .symbol:         _Z15k3_pairs_slicedPKDv4_jPKfPKiS5_PiPf.kd
    .uniform_work_group_size: 1
    .uses_dynamic_stack: false
    .vgpr_count:     101
    .vgpr_spill_count: 0
    .wavefront_size: 64
  - .agpr_count:     0
    .args:
      - .actual_access:  read_only
        .address_space:  global
        .offset:         0
        .size:           8
        .value_kind:     global_buffer
      - .actual_access:  read_only
        .address_space:  global
        .offset:         8
        .size:           8
        .value_kind:     global_buffer
      - .actual_access:  read_only
        .address_space:  global
        .offset:         16
        .size:           8
        .value_kind:     global_buffer
      - .actual_access:  read_only
        .address_space:  global
        .offset:         24
        .size:           8
        .value_kind:     global_buffer
      - .address_space:  global
        .offset:         32
        .size:           8
        .value_kind:     global_buffer
    .group_segment_fixed_size: 64
    .kernarg_segment_align: 8
    .kernarg_segment_size: 40
    .language:       OpenCL C
    .language_version:
      - 2
      - 0
    .max_flat_workgroup_size: 1024
    .name:           _Z10k4_combinePKiPKfS2_S2_Pf
    .private_segment_fixed_size: 0
    .sgpr_count:     18
    .sgpr_spill_count: 0
    .symbol:         _Z10k4_combinePKiPKfS2_S2_Pf.kd
    .uniform_work_group_size: 1
    .uses_dynamic_stack: false
    .vgpr_count:     18
    .vgpr_spill_count: 0
    .wavefront_size: 64
